# NA units: rpb bias LDS lookups batched (15 in flight, -inf sentinel entry), exp/sum/cvt block and next-tile global loads moved ahead of QK, K-fragment reads 3 deep; quant row loads issued up front
# speedup vs baseline: 1.0404x; 1.0032x over previous
.LBB0_609:
	s_or_b64 exec, exec, s[0:1]
	v_mov_b32_e32 v0, 0x11744
	ds_write_b32 v0, v217
	s_lshl_b32 s19, s7, 2
	s_max_i32 s0, s19, 4
	s_lshl_b32 s2, s7, 8
	s_add_i32 s0, s0, -4
	s_min_u32 s12, s0, 0xf4
	s_ashr_i32 s3, s2, 31
	s_lshl_b32 s13, s12, 6
	s_mul_i32 s7, s7, 0x240000
	v_writelane_b32 v255, s2, 10
	s_mul_hi_i32 s0, s2, 0x2400
	v_ashrrev_i32_e32 v18, 4, v48
	v_writelane_b32 v255, s3, 11
	s_add_u32 s2, s34, s7
	s_addc_u32 s3, s35, s0
	s_lshl_b32 s0, s6, 7
	s_ashr_i32 s1, s0, 31
	s_lshl_b64 s[4:5], s[0:1], 1
	s_add_u32 s0, s2, s4
	s_addc_u32 s1, s3, s5
	v_readlane_b32 s2, v254, 51
	s_add_u32 s14, s2, s4
	v_readlane_b32 s2, v254, 52
	s_addc_u32 s15, s2, s5
	v_readlane_b32 s2, v254, 53
	s_add_u32 s16, s2, s4
	v_readlane_b32 s2, v254, 54
	v_writelane_b32 v255, s4, 12
	s_addc_u32 s17, s2, s5
	s_add_i32 s20, 0, 0x10000
	s_cmp_lg_u32 0, -1
	s_mul_i32 s2, s12, 0x90000
	v_lshlrev_b32_e32 v19, 3, v48
	s_cselect_b32 s21, 0, 0
	s_add_u32 s36, s14, s2
	v_and_b32_e32 v20, 0x78, v19
	v_mul_lo_u32 v0, v18, s68
	s_addc_u32 s37, s15, 0
	v_or_b32_e32 v0, v0, v20
	s_add_u32 s42, s16, s2
	v_lshlrev_b32_e32 v192, 1, v0
	s_addc_u32 s43, s17, 0
	s_waitcnt lgkmcnt(0)
	s_barrier
	v_add_u32_e32 v150, 0x48000, v192
	global_load_dwordx4 v[0:3], v192, s[42:43]
	global_load_dwordx4 v[4:7], v150, s[42:43]
	global_load_dwordx4 v[8:11], v192, s[36:37]
	global_load_dwordx4 v[12:15], v150, s[36:37]
	v_ashrrev_i32_e32 v49, 1, v48
	v_bfe_u32 v154, v48, 5, 1
	v_bfi_b32 v21, s67, v49, v48
	v_mov_b64_e32 v[16:17], s[0:1]
	v_mad_i64_i32 v[16:17], s[0:1], v21, s66, v[16:17]
	v_lshlrev_b32_e32 v148, 4, v154
	v_mov_b32_e32 v149, v193
	v_lshl_add_u64 v[16:17], v[16:17], 0, v[148:149]
	global_load_dwordx4 v[100:103], v[16:17], off
	global_load_dwordx4 v[104:107], v[16:17], off offset:32
	global_load_dwordx4 v[120:123], v[16:17], off offset:64
	global_load_dwordx4 v[124:127], v[16:17], off offset:96
	global_load_dwordx4 v[116:119], v[16:17], off offset:128
	global_load_dwordx4 v[112:115], v[16:17], off offset:160
	global_load_dwordx4 v[108:111], v[16:17], off offset:192
	global_load_dwordx4 v[96:99], v[16:17], off offset:224
	v_and_b32_e32 v22, 0xfffff0, v18
	v_lshlrev_b32_e32 v23, 1, v18
	v_lshrrev_b32_e32 v24, 1, v18
	v_and_b32_e32 v25, 3, v18
	v_add_u32_e32 v26, 32, v18
	v_and_or_b32 v22, v23, 8, v22
	v_and_or_b32 v23, v24, 4, v25
	v_and_b32_e32 v24, 0xfffff0, v26
	v_lshlrev_b32_e32 v25, 1, v26
	v_and_b32_e32 v21, 0xf0, v48
	v_bfe_u32 v19, v19, 5, 2
	v_lshlrev_b32_e32 v18, 8, v18
	v_lshlrev_b32_e32 v20, 1, v20
	v_lshlrev_b32_e32 v26, 8, v26
	v_lshrrev_b32_e32 v22, 1, v22
	v_and_or_b32 v24, v25, 8, v24
	v_and_b32_e32 v27, 48, v20
	v_bitop3_b32 v18, v20, v18, v21 bitop3:0xde
	v_bitop3_b32 v20, v20, v26, v21 bitop3:0xde
	v_or_b32_e32 v21, v22, v19
	v_lshrrev_b32_e32 v22, 1, v24
	v_lshlrev_b32_e32 v23, 6, v23
	v_add_u32_e32 v153, 0, v18
	v_lshlrev_b32_e32 v18, 9, v21
	v_or_b32_e32 v19, v22, v19
	v_and_b32_e32 v149, 31, v48
	v_lshlrev_b32_e32 v50, 4, v48
	v_or3_b32 v18, v18, v23, v27
	v_lshlrev_b32_e32 v19, 9, v19
	v_lshlrev_b32_e32 v40, 8, v149
	v_or3_b32 v19, v19, v23, v27
	v_add_u32_e32 v156, 0, v18
	v_and_b32_e32 v41, 0xf0, v50
	v_add_u32_e32 v155, 0, v20
	v_add_u32_e32 v157, 0, v19
	s_waitcnt vmcnt(0)
	v_or_b32_e32 v36, 64, v148
	v_bitop3_b32 v36, v36, v40, v41 bitop3:0xde
	v_add_u32_e32 v162, 0, v36
	v_or_b32_e32 v36, 0x60, v148
	v_bitop3_b32 v36, v36, v40, v41 bitop3:0xde
	s_waitcnt vmcnt(11)
	ds_write_b128 v156, v[0:3]
	s_waitcnt vmcnt(10)
	ds_write_b128 v157, v[4:7]
	s_waitcnt vmcnt(9)
	ds_write_b128 v153, v[8:11] offset:32768
	s_waitcnt vmcnt(8)
	ds_write_b128 v155, v[12:15] offset:32768
	v_bitop3_b32 v0, v148, v40, v41 bitop3:0xde
	v_add_u32_e32 v158, 0, v0
	s_waitcnt lgkmcnt(0)
	s_barrier
	ds_read_b128 v[0:3], v158 offset:32768
	v_or_b32_e32 v4, 32, v148
	v_bitop3_b32 v32, v4, v40, v41 bitop3:0xde
	v_add_u32_e32 v161, 0, v32
	ds_read_b128 v[32:35], v161 offset:32768
	s_waitcnt vmcnt(7) lgkmcnt(1)
	v_mfma_f32_32x32x16_bf16 v[16:31], v[0:3], v[100:103], 0
	ds_read_b128 v[0:3], v158 offset:40960
	v_add_u32_e32 v160, 0, v36
	v_or_b32_e32 v36, 0x80, v148
	v_bitop3_b32 v36, v36, v40, v41 bitop3:0xde
	v_add_u32_e32 v166, 0, v36
	ds_read_b128 v[36:39], v166 offset:32768
	v_or_b32_e32 v43, 0xc0, v148
	s_waitcnt vmcnt(6) lgkmcnt(2)
	v_mfma_f32_32x32x16_bf16 v[16:31], v[32:35], v[104:107], v[16:31]
	ds_read_b128 v[32:35], v161 offset:40960
	v_ashrrev_i32_e32 v51, 7, v48
	v_add_u32_e32 v42, s19, v51
	v_max_i32_e32 v44, 4, v42
	v_and_or_b32 v168, v49, 32, v149
	v_sub_u32_e64 v45, v168, 8 clamp
	v_min_u32_e32 v54, 48, v45
	s_waitcnt lgkmcnt(2)
	v_mfma_f32_32x32x16_bf16 v[0:15], v[0:3], v[100:103], 0
	v_lshlrev_b32_e32 v173, 2, v154
	v_writelane_b32 v255, s5, 13
	v_or_b32_e32 v174, 1, v173
	v_sub_u32_e32 v52, s12, v42
	v_max_i32_e32 v52, -7, v52
	v_or_b32_e32 v175, 2, v173
	v_add_u32_e32 v52, 7, v52
	s_waitcnt lgkmcnt(0)
	v_mfma_f32_32x32x16_bf16 v[0:15], v[32:35], v[104:107], v[0:15]
	ds_read_b128 v[32:35], v162 offset:32768
	v_cmp_ge_u32_e64 s[2:3], v175, v54
	v_min_u32_e32 v52, 14, v52
	v_or_b32_e32 v176, 3, v173
	v_mul_u32_u24_e32 v52, 31, v52
	v_cmp_ge_u32_e64 s[4:5], v176, v54
	v_sub_u32_e32 v52, v52, v168
	s_waitcnt vmcnt(5) lgkmcnt(0)
	v_mfma_f32_32x32x16_bf16 v[16:31], v[32:35], v[120:123], v[16:31]
	ds_read_b128 v[32:35], v162 offset:40960
	v_or_b32_e32 v177, 8, v173
	v_add_u32_e32 v52, 15, v52
	v_cmp_ge_u32_e64 s[6:7], v177, v54
	v_add_u32_e32 v53, v52, v173
	v_or_b32_e32 v178, 9, v173
	s_add_i32 s18, 0, 0x11000
	s_waitcnt lgkmcnt(0)
	v_mfma_f32_32x32x16_bf16 v[0:15], v[32:35], v[120:123], v[0:15]
	ds_read_b128 v[32:35], v160 offset:32768
	v_cmp_ge_u32_e64 s[8:9], v178, v54
	v_or_b32_e32 v179, 10, v173
	v_cmp_ge_u32_e64 s[22:23], v179, v54
	v_or_b32_e32 v180, 11, v173
	v_add_u32_e32 v60, v52, v178
	v_add_u32_e32 v61, v52, v179
	s_waitcnt vmcnt(4) lgkmcnt(0)
	v_mfma_f32_32x32x16_bf16 v[16:31], v[32:35], v[124:127], v[16:31]
	ds_read_b128 v[32:35], v160 offset:40960
	v_add_u32_e32 v62, v52, v180
	v_or_b32_e32 v181, 16, v173
	v_or_b32_e32 v182, 17, v173
	v_or_b32_e32 v183, 18, v173
	v_or_b32_e32 v184, 19, v173
	v_or_b32_e32 v185, 24, v173
	s_waitcnt lgkmcnt(0)
	v_mfma_f32_32x32x16_bf16 v[0:15], v[32:35], v[124:127], v[0:15]
	v_or_b32_e32 v32, 0xa0, v148
	v_bitop3_b32 v32, v32, v40, v41 bitop3:0xde
	v_add_u32_e32 v165, 0, v32
	ds_read_b128 v[32:35], v165 offset:32768
	v_or_b32_e32 v186, 25, v173
	v_cmp_ge_u32_e64 s[34:35], v186, v54
	v_or_b32_e32 v187, 26, v173
	s_waitcnt vmcnt(3)
	v_mfma_f32_32x32x16_bf16 v[16:31], v[36:39], v[116:119], v[16:31]
	v_bitop3_b32 v37, v43, v40, v41 bitop3:0xde
	v_or_b32_e32 v36, 0xe0, v148
	v_add_u32_e32 v164, 0, v37
	v_bitop3_b32 v40, v36, v40, v41 bitop3:0xde
	ds_read_b128 v[36:39], v164 offset:32768
	v_add_u32_e32 v163, 0, v40
	ds_read_b128 v[56:59], v163 offset:32768
	s_waitcnt vmcnt(2) lgkmcnt(2)
	v_mfma_f32_32x32x16_bf16 v[16:31], v[32:35], v[112:115], v[16:31]
	v_add_u32_e32 v32, -4, v44
	v_min_u32_e32 v169, 0xf8, v32
	v_add_u32_e32 v170, 8, v169
	v_cmp_ge_u32_e32 vcc, s12, v32
	v_cmp_lt_u32_e64 s[0:1], s12, v170
	s_and_b64 s[10:11], vcc, s[0:1]
	v_cmp_ge_u32_e64 s[0:1], v173, v54
	s_waitcnt vmcnt(1) lgkmcnt(1)
	v_mfma_f32_32x32x16_bf16 v[16:31], v[36:39], v[108:111], v[16:31]
	ds_read_b128 v[44:47], v166 offset:40960
	ds_read_b128 v[40:43], v165 offset:40960
	ds_read_b128 v[32:35], v164 offset:40960
	ds_read_b128 v[36:39], v163 offset:40960
	v_writelane_b32 v255, s0, 14
	s_and_b64 vcc, s[0:1], s[10:11]
	v_cndmask_b32_e32 v53, 0, v53, vcc
	v_writelane_b32 v255, s1, 15
	v_cmp_ge_u32_e64 s[0:1], v174, v54
	v_lshl_add_u32 v55, v53, 2, s18
	s_waitcnt vmcnt(0) lgkmcnt(4)
	v_mfma_f32_32x32x16_bf16 v[16:31], v[56:59], v[96:99], v[16:31]
	v_writelane_b32 v255, s0, 16
	v_add_u32_e32 v53, v52, v174
	v_add_u32_e32 v59, v52, v177
	v_writelane_b32 v255, s1, 17
	v_writelane_b32 v255, s2, 18
	s_and_b64 s[0:1], s[0:1], s[10:11]
	v_cndmask_b32_e64 v53, 0, v53, s[0:1]
	v_writelane_b32 v255, s3, 19
	v_writelane_b32 v255, s4, 20
	v_lshl_add_u32 v56, v53, 2, s18
	v_add_u32_e32 v53, v52, v175
	v_writelane_b32 v255, s5, 21
	v_writelane_b32 v255, s6, 22
	s_and_b64 s[2:3], s[2:3], s[10:11]
	v_cndmask_b32_e64 v53, 0, v53, s[2:3]
	v_writelane_b32 v255, s7, 23
	v_writelane_b32 v255, s8, 24
	v_lshl_add_u32 v57, v53, 2, s18
	v_add_u32_e32 v53, v52, v176
	v_writelane_b32 v255, s9, 25
	v_writelane_b32 v255, s22, 26
	s_and_b64 s[38:39], s[10:11], s[22:23]
	s_and_b64 s[4:5], s[4:5], s[10:11]
	v_writelane_b32 v255, s23, 27
	v_cmp_ge_u32_e64 s[22:23], v180, v54
	s_and_b64 s[6:7], s[10:11], s[6:7]
	s_and_b64 s[8:9], s[10:11], s[8:9]
	s_and_b64 s[40:41], s[10:11], s[22:23]
	v_cndmask_b32_e64 v53, 0, v53, s[4:5]
	v_cndmask_b32_e64 v59, 0, v59, s[6:7]
	v_cndmask_b32_e64 v60, 0, v60, s[8:9]
	v_cndmask_b32_e64 v61, 0, v61, s[38:39]
	v_cndmask_b32_e64 v62, 0, v62, s[40:41]
	v_lshl_add_u32 v58, v53, 2, s18
	v_lshl_add_u32 v59, v59, 2, s18
	v_lshl_add_u32 v60, v60, 2, s18
	v_lshl_add_u32 v61, v61, 2, s18
	v_lshl_add_u32 v62, v62, 2, s18
	ds_read_b32 v55, v55
	ds_read_b32 v56, v56
	ds_read_b32 v57, v57
	ds_read_b32 v58, v58
	ds_read_b32 v59, v59
	ds_read_b32 v60, v60
	ds_read_b32 v61, v61
	ds_read_b32 v62, v62
	s_waitcnt lgkmcnt(6)
	v_add_f32_e32 v17, v17, v56
	v_cndmask_b32_e64 v17, v217, v17, s[0:1]
	v_cmp_ge_u32_e64 s[0:1], v181, v54
	s_waitcnt lgkmcnt(5)
	v_add_f32_e32 v18, v18, v57
	v_cndmask_b32_e64 v18, v217, v18, s[2:3]
	v_writelane_b32 v255, s0, 28
	v_cmp_lt_u32_e64 s[2:3], v173, v54
	v_add_f32_e32 v16, v16, v55
	v_writelane_b32 v255, s1, 29
	s_and_b64 s[0:1], s[10:11], s[0:1]
	v_writelane_b32 v255, s2, 30
	v_cndmask_b32_e32 v16, v217, v16, vcc
	s_and_b64 vcc, s[0:1], s[2:3]
	v_writelane_b32 v255, s3, 31
	v_cmp_ge_u32_e64 s[0:1], v182, v54
	v_add_u32_e32 v53, 16, v54
	v_cmp_lt_u32_e64 s[2:3], v182, v53
	v_writelane_b32 v255, s0, 32
	s_waitcnt lgkmcnt(4)
	v_add_f32_e32 v19, v19, v58
	v_cndmask_b32_e64 v19, v217, v19, s[4:5]
	v_writelane_b32 v255, s1, 33
	s_and_b64 s[0:1], s[10:11], s[0:1]
	v_writelane_b32 v255, s2, 34
	s_and_b64 s[0:1], s[0:1], s[2:3]
	v_cmp_lt_u32_e64 s[4:5], v183, v53
	v_writelane_b32 v255, s3, 35
	v_cmp_ge_u32_e64 s[2:3], v183, v54
	s_waitcnt lgkmcnt(3)
	v_add_f32_e32 v20, v20, v59
	v_cndmask_b32_e64 v20, v217, v20, s[6:7]
	v_writelane_b32 v255, s2, 36
	v_cmp_lt_u32_e64 s[6:7], v184, v53
	v_add_u32_e32 v55, v52, v181
	v_writelane_b32 v255, s3, 37
	s_and_b64 s[2:3], s[10:11], s[2:3]
	v_writelane_b32 v255, s4, 38
	s_and_b64 s[2:3], s[2:3], s[4:5]
	v_add_u32_e32 v56, v52, v182
	v_writelane_b32 v255, s5, 39
	v_cmp_ge_u32_e64 s[4:5], v184, v54
	v_add_u32_e32 v57, v52, v183
	v_add_u32_e32 v58, v52, v184
	v_writelane_b32 v255, s4, 40
	v_cndmask_b32_e32 v55, 0, v55, vcc
	v_cndmask_b32_e64 v56, 0, v56, s[0:1]
	v_writelane_b32 v255, s5, 41
	s_and_b64 s[4:5], s[10:11], s[4:5]
	v_writelane_b32 v255, s6, 42
	s_and_b64 s[4:5], s[4:5], s[6:7]
	v_cndmask_b32_e64 v57, 0, v57, s[2:3]
	v_cndmask_b32_e64 v58, 0, v58, s[4:5]
	v_lshl_add_u32 v55, v55, 2, s18
	v_lshl_add_u32 v56, v56, 2, s18
	v_lshl_add_u32 v57, v57, 2, s18
	v_lshl_add_u32 v58, v58, 2, s18
	v_writelane_b32 v255, s7, 43
	ds_read_b32 v55, v55
	ds_read_b32 v56, v56
	ds_read_b32 v57, v57
	ds_read_b32 v58, v58
	v_cmp_ge_u32_e64 s[6:7], v185, v54
	s_waitcnt lgkmcnt(3)
	v_add_f32_e32 v24, v24, v55
	v_cmp_lt_u32_e64 s[30:31], v185, v53
	v_writelane_b32 v255, s6, 44
	v_cndmask_b32_e32 v24, v217, v24, vcc
	v_add_u32_e32 v55, v52, v185
	v_writelane_b32 v255, s7, 45
	s_and_b64 s[6:7], s[10:11], s[6:7]
	s_and_b64 vcc, s[6:7], s[30:31]
	v_cndmask_b32_e32 v55, 0, v55, vcc
	v_lshl_add_u32 v55, v55, 2, s18
	ds_read_b32 v55, v55
	s_waitcnt lgkmcnt(3)
	v_add_f32_e32 v25, v25, v56
	s_waitcnt lgkmcnt(2)
	v_add_f32_e32 v26, v26, v57
	v_cndmask_b32_e64 v25, v217, v25, s[0:1]
	v_cndmask_b32_e64 v26, v217, v26, s[2:3]
	s_and_b64 s[0:1], s[10:11], s[34:35]
	s_waitcnt lgkmcnt(0)
	v_add_f32_e32 v28, v28, v55
	v_cmp_lt_u32_e64 s[2:3], v186, v53
	v_cndmask_b32_e32 v28, v217, v28, vcc
	v_add_u32_e32 v55, v52, v186
	s_and_b64 vcc, s[0:1], s[2:3]
	v_cndmask_b32_e32 v55, 0, v55, vcc
	v_lshl_add_u32 v55, v55, 2, s18
	ds_read_b32 v55, v55
	v_mfma_f32_32x32x16_bf16 v[0:15], v[44:47], v[116:119], v[0:15]
	v_cmp_ge_u32_e64 s[0:1], v187, v54
	s_mov_b64 s[24:25], s[2:3]
	s_mov_b64 s[26:27], s[0:1]
	s_waitcnt lgkmcnt(0)
	v_add_f32_e32 v29, v29, v55
	s_and_b64 s[0:1], s[10:11], s[0:1]
	v_cmp_lt_u32_e64 s[2:3], v187, v53
	v_cndmask_b32_e32 v29, v217, v29, vcc
	v_add_u32_e32 v44, v52, v187
	s_and_b64 vcc, s[0:1], s[2:3]
	v_cndmask_b32_e32 v44, 0, v44, vcc
	v_lshl_add_u32 v44, v44, 2, s18
	v_mfma_f32_32x32x16_bf16 v[0:15], v[40:43], v[112:115], v[0:15]
	ds_read_b32 v44, v44
	v_or_b32_e32 v188, 27, v173
	v_cmp_ge_u32_e64 s[52:53], v188, v54
	s_and_b64 s[0:1], s[10:11], s[52:53]
	v_cmp_lt_u32_e64 s[54:55], v188, v53
	s_waitcnt lgkmcnt(0)
	v_add_f32_e32 v30, v30, v44
	v_cndmask_b32_e32 v30, v217, v30, vcc
	v_add_u32_e32 v40, v52, v188
	s_and_b64 vcc, s[0:1], s[54:55]
	v_cndmask_b32_e32 v40, 0, v40, vcc
	v_mfma_f32_32x32x16_bf16 v[0:15], v[32:35], v[108:111], v[0:15]
	v_lshl_add_u32 v40, v40, 2, s18
	ds_read_b32 v40, v40
	v_or_b32_e32 v189, 32, v173
	v_cmp_ge_u32_e64 s[56:57], v189, v54
	s_and_b64 s[0:1], s[10:11], s[56:57]
	v_cmp_lt_u32_e64 s[58:59], v189, v53
	s_waitcnt lgkmcnt(0)
	v_add_f32_e32 v31, v31, v40
	v_cndmask_b32_e32 v31, v217, v31, vcc
	v_add_u32_e32 v32, v52, v189
	s_and_b64 vcc, s[0:1], s[58:59]
	v_mfma_f32_32x32x16_bf16 v[0:15], v[36:39], v[96:99], v[0:15]
	v_cndmask_b32_e32 v32, 0, v32, vcc
	v_lshl_add_u32 v32, v32, 2, s18
	ds_read_b32 v32, v32
	v_or_b32_e32 v190, 33, v173
	v_cmp_ge_u32_e64 s[60:61], v190, v54
	s_and_b64 s[0:1], s[10:11], s[60:61]
	v_cmp_lt_u32_e64 s[62:63], v190, v53
	s_waitcnt lgkmcnt(0)
	s_nop 3
	v_add_f32_e32 v0, v0, v32
	v_cndmask_b32_e32 v32, v217, v0, vcc
	v_add_u32_e32 v0, v52, v190
	s_and_b64 vcc, s[0:1], s[62:63]
	v_cndmask_b32_e32 v0, 0, v0, vcc
	v_lshl_add_u32 v0, v0, 2, s18
	ds_read_b32 v0, v0
	v_or_b32_e32 v191, 34, v173
	v_cmp_ge_u32_e64 s[64:65], v191, v54
	s_and_b64 s[0:1], s[10:11], s[64:65]
	v_cmp_lt_u32_e64 s[66:67], v191, v53
	s_waitcnt lgkmcnt(0)
	v_add_f32_e32 v0, v1, v0
	v_cndmask_b32_e32 v33, v217, v0, vcc
	v_add_u32_e32 v0, v52, v191
	s_and_b64 vcc, s[0:1], s[66:67]
	v_cndmask_b32_e32 v0, 0, v0, vcc
	v_lshl_add_u32 v0, v0, 2, s18
	ds_read_b32 v0, v0
	v_or_b32_e32 v200, 35, v173
	v_cmp_ge_u32_e64 s[68:69], v200, v54
	s_and_b64 s[0:1], s[10:11], s[68:69]
	v_cmp_lt_u32_e64 s[70:71], v200, v53
	s_waitcnt lgkmcnt(0)
	v_add_f32_e32 v0, v2, v0
	v_cndmask_b32_e32 v34, v217, v0, vcc
	v_add_u32_e32 v0, v52, v200
	s_and_b64 vcc, s[0:1], s[70:71]
	v_cndmask_b32_e32 v0, 0, v0, vcc
	v_lshl_add_u32 v0, v0, 2, s18
	ds_read_b32 v0, v0
	v_or_b32_e32 v201, 40, v173
	v_cmp_ge_u32_e64 s[72:73], v201, v54
	s_and_b64 s[0:1], s[10:11], s[72:73]
	v_cmp_lt_u32_e64 s[74:75], v201, v53
	s_waitcnt lgkmcnt(0)
	v_add_f32_e32 v0, v3, v0
	v_cndmask_b32_e32 v35, v217, v0, vcc
	v_add_u32_e32 v0, v52, v201
	s_and_b64 vcc, s[0:1], s[74:75]
	v_cndmask_b32_e32 v0, 0, v0, vcc
	v_lshl_add_u32 v0, v0, 2, s18
	ds_read_b32 v0, v0
	v_or_b32_e32 v203, 41, v173
	v_cmp_ge_u32_e64 s[76:77], v203, v54
	s_and_b64 s[0:1], s[10:11], s[76:77]
	v_cmp_lt_u32_e64 s[78:79], v203, v53
	s_waitcnt lgkmcnt(0)
	v_add_f32_e32 v0, v4, v0
	v_cndmask_b32_e32 v36, v217, v0, vcc
	v_add_u32_e32 v0, v52, v203
	s_and_b64 vcc, s[0:1], s[78:79]
	v_cndmask_b32_e32 v0, 0, v0, vcc
	v_lshl_add_u32 v0, v0, 2, s18
	ds_read_b32 v0, v0
	v_or_b32_e32 v204, 42, v173
	v_cmp_ge_u32_e64 s[80:81], v204, v54
	s_and_b64 s[0:1], s[10:11], s[80:81]
	v_cmp_lt_u32_e64 s[82:83], v204, v53
	s_waitcnt lgkmcnt(0)
	v_add_f32_e32 v0, v5, v0
	v_cndmask_b32_e32 v37, v217, v0, vcc
	v_add_u32_e32 v0, v52, v204
	s_and_b64 vcc, s[0:1], s[82:83]
	v_cndmask_b32_e32 v0, 0, v0, vcc
	v_lshl_add_u32 v0, v0, 2, s18
	ds_read_b32 v0, v0
	v_or_b32_e32 v205, 43, v173
	v_cmp_ge_u32_e64 s[84:85], v205, v54
	s_and_b64 s[0:1], s[10:11], s[84:85]
	v_cmp_lt_u32_e64 s[86:87], v205, v53
	s_waitcnt lgkmcnt(0)
	v_add_f32_e32 v0, v6, v0
	v_cndmask_b32_e32 v46, v217, v0, vcc
	v_add_u32_e32 v0, v52, v205
	s_and_b64 vcc, s[0:1], s[86:87]
	v_cndmask_b32_e32 v0, 0, v0, vcc
	v_lshl_add_u32 v0, v0, 2, s18
	ds_read_b32 v0, v0
	v_or_b32_e32 v206, 48, v173
	v_cmp_lt_u32_e64 s[88:89], v206, v53
	v_or_b32_e32 v207, 49, v173
	s_waitcnt lgkmcnt(0)
	v_add_f32_e32 v0, v7, v0
	v_cndmask_b32_e32 v47, v217, v0, vcc
	v_add_u32_e32 v0, v52, v206
	s_and_b64 vcc, s[10:11], s[88:89]
	v_cndmask_b32_e32 v0, 0, v0, vcc
	v_lshl_add_u32 v0, v0, 2, s18
	ds_read_b32 v0, v0
	v_cmp_lt_u32_e64 s[90:91], v207, v53
	v_add_f32_e32 v21, v21, v60
	v_or_b32_e32 v208, 50, v173
	v_cmp_lt_u32_e64 s[92:93], v208, v53
	s_waitcnt lgkmcnt(0)
	v_add_f32_e32 v0, v8, v0
	v_cndmask_b32_e32 v60, v217, v0, vcc
	v_add_u32_e32 v0, v52, v207
	s_and_b64 vcc, s[10:11], s[90:91]
	v_cndmask_b32_e32 v0, 0, v0, vcc
	v_lshl_add_u32 v0, v0, 2, s18
	ds_read_b32 v0, v0
	v_add_f32_e32 v22, v22, v61
	v_or_b32_e32 v209, 51, v173
	v_cmp_lt_u32_e64 s[94:95], v209, v53
	v_add_f32_e32 v23, v23, v62
	s_waitcnt lgkmcnt(0)
	v_add_f32_e32 v0, v9, v0
	v_cndmask_b32_e32 v61, v217, v0, vcc
	v_add_u32_e32 v0, v52, v208
	s_and_b64 vcc, s[10:11], s[92:93]
	v_cndmask_b32_e32 v0, 0, v0, vcc
	v_lshl_add_u32 v0, v0, 2, s18
	ds_read_b32 v0, v0
	v_or_b32_e32 v210, 56, v173
	v_cmp_lt_u32_e64 s[96:97], v210, v53
	v_or_b32_e32 v211, 57, v173
	s_mov_b64 s[28:29], s[2:3]
	s_waitcnt lgkmcnt(0)
	v_add_f32_e32 v0, v10, v0
	v_cndmask_b32_e32 v62, v217, v0, vcc
	v_add_u32_e32 v0, v52, v209
	s_and_b64 vcc, s[10:11], s[94:95]
	v_cndmask_b32_e32 v0, 0, v0, vcc
	v_lshl_add_u32 v0, v0, 2, s18
	ds_read_b32 v0, v0
	v_cmp_lt_u32_e64 s[2:3], v211, v53
	v_or_b32_e32 v212, 58, v173
	v_cmp_lt_u32_e64 s[0:1], v212, v53
	s_waitcnt lgkmcnt(0)
	v_add_f32_e32 v0, v11, v0
	v_cndmask_b32_e32 v63, v217, v0, vcc
	v_add_u32_e32 v0, v52, v210
	s_and_b64 vcc, s[10:11], s[96:97]
	v_cndmask_b32_e32 v0, 0, v0, vcc
	v_lshl_add_u32 v0, v0, 2, s18
	ds_read_b32 v0, v0
	v_or_b32_e32 v213, 59, v173
	v_cmp_lt_u32_e64 s[6:7], v213, v53
	v_cndmask_b32_e64 v21, v217, v21, s[8:9]
	v_cndmask_b32_e64 v22, v217, v22, s[38:39]
	s_waitcnt lgkmcnt(0)
	v_add_f32_e32 v0, v12, v0
	v_cndmask_b32_e32 v64, v217, v0, vcc
	v_add_u32_e32 v0, v52, v211
	s_and_b64 vcc, s[10:11], s[2:3]
	v_cndmask_b32_e32 v0, 0, v0, vcc
	v_lshl_add_u32 v0, v0, 2, s18
	ds_read_b32 v0, v0
	v_cndmask_b32_e64 v23, v217, v23, s[40:41]
	v_add_f32_e32 v27, v27, v58
	v_cndmask_b32_e64 v27, v217, v27, s[4:5]
	s_mov_b32 s4, 0x42b504f3
	s_waitcnt lgkmcnt(0)
	v_add_f32_e32 v0, v13, v0
	v_cndmask_b32_e32 v65, v217, v0, vcc
	v_add_u32_e32 v0, v52, v212
	s_and_b64 vcc, s[10:11], s[0:1]
	v_cndmask_b32_e32 v0, 0, v0, vcc
	v_lshl_add_u32 v0, v0, 2, s18
	ds_read_b32 v0, v0
	v_mov_b32_e32 v2, 0xf149f2ca
	v_and_b32_e32 v68, 63, v48
	v_and_b32_e32 v152, 0xffffffe0, v49
	v_mov_b32_e32 v194, 0x8000
	s_waitcnt lgkmcnt(0)
	v_add_f32_e32 v0, v14, v0
	v_cndmask_b32_e32 v66, v217, v0, vcc
	v_add_u32_e32 v0, v52, v213
	s_and_b64 vcc, s[10:11], s[6:7]
	v_cndmask_b32_e32 v0, 0, v0, vcc
	v_lshl_add_u32 v0, v0, 2, s18
	ds_read_b32 v0, v0
	v_mov_b32_e32 v216, 0xc000
	v_mov_b32_e32 v151, v193
	s_waitcnt lgkmcnt(0)
	v_add_f32_e32 v0, v15, v0
	v_cndmask_b32_e32 v67, v217, v0, vcc
	v_max_f32_e32 v0, v16, v17
	v_max3_f32 v0, v0, v18, v19
	v_max3_f32 v0, v0, v20, v21
	v_max3_f32 v0, v0, v22, v23
	v_max3_f32 v0, v0, v24, v25
	v_max3_f32 v0, v0, v26, v27
	v_max3_f32 v0, v0, v28, v29
	v_max3_f32 v0, v0, v30, v31
	v_max3_f32 v0, v0, v32, v33
	v_max3_f32 v0, v0, v34, v35
	v_max3_f32 v0, v0, v36, v37
	v_max3_f32 v0, v0, v46, v47
	v_max3_f32 v0, v0, v60, v61
	v_max3_f32 v0, v0, v62, v63
	v_max3_f32 v0, v0, v64, v65
	v_max3_f32 v0, v0, v66, v67
	v_mov_b32_e32 v1, v0
	s_nop 1
	v_permlane32_swap_b32_e32 v0, v1
	v_max_f32_e32 v1, v1, v1
	v_max_f32_e32 v0, v0, v0
	v_max_f32_e32 v0, v0, v1
	v_add_f32_e32 v1, 0x7149f2ca, v0
	v_cmp_ge_f32_e32 vcc, s4, v1
	s_cmp_eq_u64 vcc, exec
	s_cselect_b64 vcc, -1, 0
	s_add_u32 s4, s36, 0x90000
	s_addc_u32 s5, s37, 0
	s_add_u32 s8, s42, 0x90000
	s_addc_u32 s9, s43, 0
	global_load_dwordx4 v[38:41], v150, s[8:9]
	global_load_dwordx4 v[42:45], v192, s[8:9]
	global_load_dwordx4 v[52:55], v192, s[4:5]
	global_load_dwordx4 v[56:59], v150, s[4:5]
	v_max_f32_e32 v0, 0xf149f2ca, v0
	v_sub_f32_e32 v1, 0xf149f2ca, v0
	v_mul_f32_e32 v1, 0x3e0293ee, v1
	v_exp_f32_e32 v1, v1
	v_cndmask_b32_e32 v222, v0, v2, vcc
	v_and_b32_e32 v0, 0x3fffffc0, v48
	v_lshl_add_u32 v159, v0, 2, s20
	v_cndmask_b32_e64 v214, v1, 1.0, vcc
	v_lshlrev_b32_e32 v0, 3, v68
	v_and_b32_e32 v1, 0xc0, v50
	v_lshlrev_b32_e32 v2, 1, v48
	v_and_or_b32 v1, v0, 24, v1
	v_and_b32_e32 v2, 32, v2
	v_and_b32_e32 v0, 0x100, v0
	v_or3_b32 v0, v1, v2, v0
	v_readlane_b32 s36, v254, 57
	v_add_u32_e32 v202, s21, v0
	s_addk_i32 s21, 0x4000
	v_readlane_b32 s37, v254, 58
	v_add_u32_e32 v167, s21, v0
	v_sub_u32_e32 v0, s12, v51
	s_mov_b32 s5, s37
	v_subrev_u32_e32 v215, s19, v0
	v_readlane_b32 s38, v254, 59
	v_readlane_b32 s39, v254, 60
	v_readlane_b32 s40, v254, 61
	v_readlane_b32 s41, v254, 62
	v_readlane_b32 s42, v254, 63
	v_readlane_b32 s43, v255, 0
	v_readlane_b32 s44, v255, 1
	v_readlane_b32 s45, v255, 2
	v_readlane_b32 s46, v255, 3
	v_readlane_b32 s47, v255, 4
	v_readlane_b32 s48, v255, 5
	v_readlane_b32 s49, v255, 6
	v_readlane_b32 s50, v255, 7
	v_readlane_b32 s51, v255, 8
	v_writelane_b32 v254, s4, 57
	v_mul_f32_e32 v129, 0xbe0293ee, v222
	s_mov_b32 s36, s37
	v_writelane_b32 v255, s11, 0
	v_writelane_b32 v255, s12, 1
	v_writelane_b32 v255, s13, 2
	v_writelane_b32 v255, s14, 3
	v_writelane_b32 v255, s15, 4
	v_writelane_b32 v254, s5, 58
	v_writelane_b32 v255, s16, 5
	v_writelane_b32 v254, s6, 59
	v_writelane_b32 v255, s17, 6
	v_fmamk_f32 v16, v16, 0x3e0293ee, v129
	v_fmamk_f32 v17, v17, 0x3e0293ee, v129
	v_fmamk_f32 v18, v18, 0x3e0293ee, v129
	v_fmamk_f32 v19, v19, 0x3e0293ee, v129
	v_fmamk_f32 v20, v20, 0x3e0293ee, v129
	v_fmamk_f32 v21, v21, 0x3e0293ee, v129
	v_fmamk_f32 v22, v22, 0x3e0293ee, v129
	v_fmamk_f32 v23, v23, 0x3e0293ee, v129
	v_fmamk_f32 v24, v24, 0x3e0293ee, v129
	v_fmamk_f32 v25, v25, 0x3e0293ee, v129
	v_fmamk_f32 v26, v26, 0x3e0293ee, v129
	v_fmamk_f32 v27, v27, 0x3e0293ee, v129
	v_fmamk_f32 v28, v28, 0x3e0293ee, v129
	v_fmamk_f32 v29, v29, 0x3e0293ee, v129
	v_fmamk_f32 v30, v30, 0x3e0293ee, v129
	v_fmamk_f32 v31, v31, 0x3e0293ee, v129
	s_mov_b32 s38, s37
	s_mov_b32 s39, s37
	s_mov_b32 s40, s37
	s_mov_b32 s41, s37
	s_mov_b32 s42, s37
	s_mov_b32 s43, s37
	s_mov_b32 s44, s37
	s_mov_b32 s45, s37
	s_mov_b32 s46, s37
	s_mov_b32 s47, s37
	s_mov_b32 s48, s37
	s_mov_b32 s49, s37
	s_mov_b32 s50, s37
	s_mov_b32 s51, s37
	v_writelane_b32 v254, s7, 60
	v_writelane_b32 v255, s18, 7
	v_mov_b64_e32 v[0:1], s[36:37]
	v_exp_f32_e32 v236, v16
	v_exp_f32_e32 v238, v17
	v_exp_f32_e32 v145, v18
	v_exp_f32_e32 v237, v19
	v_exp_f32_e32 v146, v20
	v_exp_f32_e32 v235, v21
	v_exp_f32_e32 v147, v22
	v_exp_f32_e32 v234, v23
	v_exp_f32_e32 v231, v24
	v_exp_f32_e32 v233, v25
	v_exp_f32_e32 v230, v26
	v_exp_f32_e32 v232, v27
	v_exp_f32_e32 v227, v28
	v_exp_f32_e32 v229, v29
	v_exp_f32_e32 v226, v30
	v_exp_f32_e32 v228, v31
	v_writelane_b32 v254, s8, 61
	v_writelane_b32 v255, s19, 8
	v_mov_b64_e32 v[14:15], s[50:51]
	s_waitcnt vmcnt(0)
	v_writelane_b32 v254, s9, 62
	v_mov_b64_e32 v[2:3], s[38:39]
	v_mov_b64_e32 v[4:5], s[40:41]
	v_mov_b64_e32 v[6:7], s[42:43]
	v_mov_b64_e32 v[8:9], s[44:45]
	v_mov_b64_e32 v[10:11], s[46:47]
	v_mov_b64_e32 v[12:13], s[48:49]
	v_readlane_b32 s48, v255, 26
	v_readlane_b32 s46, v255, 24
	v_readlane_b32 s44, v255, 22
	v_readlane_b32 s42, v255, 20
	v_readlane_b32 s40, v255, 18
	v_readlane_b32 s38, v255, 16
	v_readlane_b32 s36, v255, 14
	v_fmamk_f32 v134, v32, 0x3e0293ee, v129
	v_fmamk_f32 v135, v33, 0x3e0293ee, v129
	v_fmamk_f32 v138, v34, 0x3e0293ee, v129
	v_fmamk_f32 v139, v35, 0x3e0293ee, v129
	v_fmamk_f32 v130, v36, 0x3e0293ee, v129
	v_fmamk_f32 v131, v37, 0x3e0293ee, v129
	v_fmamk_f32 v132, v46, 0x3e0293ee, v129
	v_fmamk_f32 v133, v47, 0x3e0293ee, v129
	v_fmamk_f32 v136, v60, 0x3e0293ee, v129
	v_fmamk_f32 v137, v61, 0x3e0293ee, v129
	v_fmamk_f32 v142, v62, 0x3e0293ee, v129
	v_fmamk_f32 v143, v63, 0x3e0293ee, v129
	s_waitcnt vmcnt(2)
	ds_write_b128 v156, v[42:45] offset:16384
	ds_write_b128 v157, v[38:41] offset:16384
	s_waitcnt vmcnt(1)
	ds_write_b128 v153, v[52:55] offset:49152
	s_waitcnt vmcnt(0)
	ds_write_b128 v155, v[56:59] offset:49152
	v_mov_b64_e32 v[62:63], v[14:15]
	v_mov_b64_e32 v[46:47], v[14:15]
	v_mov_b64_e32 v[30:31], v[14:15]
	v_writelane_b32 v254, s10, 63
	s_mov_b64 s[50:51], s[22:23]
	v_readlane_b32 s49, v255, 27
	v_readlane_b32 s47, v255, 25
	v_readlane_b32 s45, v255, 23
	v_readlane_b32 s43, v255, 21
	v_readlane_b32 s41, v255, 19
	v_readlane_b32 s39, v255, 17
	v_readlane_b32 s37, v255, 15
	v_fmamk_f32 v140, v64, 0x3e0293ee, v129
	v_fmamk_f32 v141, v65, 0x3e0293ee, v129
	v_fmamk_f32 v128, v66, 0x3e0293ee, v129
	v_fmac_f32_e32 v129, 0x3e0293ee, v67
	v_lshl_add_u32 v171, v149, 2, v159
	v_mov_b32_e32 v172, 0
	v_mov_b64_e32 v[60:61], v[12:13]
	v_mov_b64_e32 v[58:59], v[10:11]
	v_mov_b64_e32 v[56:57], v[8:9]
	v_mov_b64_e32 v[54:55], v[6:7]
	v_mov_b64_e32 v[52:53], v[4:5]
	v_mov_b64_e32 v[50:51], v[2:3]
	v_mov_b64_e32 v[48:49], v[0:1]
	v_mov_b64_e32 v[44:45], v[12:13]
	v_mov_b64_e32 v[42:43], v[10:11]
	v_mov_b64_e32 v[40:41], v[8:9]
	v_mov_b64_e32 v[38:39], v[6:7]
	v_mov_b64_e32 v[36:37], v[4:5]
	v_mov_b64_e32 v[34:35], v[2:3]
	v_mov_b64_e32 v[32:33], v[0:1]
	v_mov_b64_e32 v[28:29], v[12:13]
	v_mov_b64_e32 v[26:27], v[10:11]
	v_mov_b64_e32 v[24:25], v[8:9]
	v_mov_b64_e32 v[22:23], v[6:7]
	v_mov_b64_e32 v[20:21], v[4:5]
	v_mov_b64_e32 v[18:19], v[2:3]
	v_mov_b64_e32 v[16:17], v[0:1]
	s_mov_b32 s19, -1
	v_cmp_gt_u32_e64 s[4:5], 32, v68
	s_waitcnt lgkmcnt(0)
	s_barrier
.LBB0_610:
	s_add_i32 s20, s19, 2
	ds_read_b128 v[64:67], v158 offset:49152
	ds_read_b128 v[240:243], v161 offset:49152
	ds_read_b128 v[244:247], v158 offset:57344
	ds_read_b128 v[248:251], v161 offset:57344
	v_add_f32_e32 v144, 0, v236
	v_add_f32_e32 v144, v238, v144
	v_add_f32_e32 v144, v145, v144
	v_add_f32_e32 v144, v237, v144
	v_add_f32_e32 v144, v146, v144
	v_add_f32_e32 v144, v235, v144
	v_add_f32_e32 v144, v147, v144
	v_add_f32_e32 v144, v234, v144
	v_add_f32_e32 v144, v231, v144
	v_add_f32_e32 v144, v233, v144
	v_add_f32_e32 v144, v230, v144
	v_add_f32_e32 v144, v232, v144
	v_exp_f32_e32 v134, v134
	v_add_f32_e32 v144, v227, v144
	v_exp_f32_e32 v135, v135
	v_add_f32_e32 v144, v229, v144
	v_exp_f32_e32 v138, v138
	v_add_f32_e32 v144, v226, v144
	v_exp_f32_e32 v139, v139
	v_add_f32_e32 v144, v228, v144
	v_exp_f32_e32 v130, v130
	v_add_f32_e32 v144, v134, v144
	v_exp_f32_e32 v131, v131
	v_add_f32_e32 v144, v135, v144
	v_exp_f32_e32 v132, v132
	v_add_f32_e32 v144, v138, v144
	v_exp_f32_e32 v133, v133
	v_add_f32_e32 v144, v139, v144
	v_exp_f32_e32 v136, v136
	v_add_f32_e32 v144, v130, v144
	v_exp_f32_e32 v137, v137
	v_add_f32_e32 v144, v131, v144
	v_exp_f32_e32 v142, v142
	v_add_f32_e32 v144, v132, v144
	v_exp_f32_e32 v143, v143
	v_add_f32_e32 v144, v133, v144
	v_exp_f32_e32 v140, v140
	v_add_f32_e32 v144, v136, v144
	v_exp_f32_e32 v141, v141
	v_add_f32_e32 v144, v137, v144
	v_exp_f32_e32 v128, v128
	v_add_f32_e32 v144, v142, v144
	v_exp_f32_e32 v129, v129
	v_add_f32_e32 v144, v143, v144
	v_add_f32_e32 v144, v140, v144
	v_add_f32_e32 v144, v141, v144
	v_add_f32_e32 v144, v128, v144
	v_add_f32_e32 v223, v129, v144
	v_mov_b32_e32 v224, v223
	v_cvt_pk_bf16_f32 v144, v236, v238
	v_cvt_pk_bf16_f32 v145, v145, v237
	v_cvt_pk_bf16_f32 v146, v146, v235
	s_nop 0
	v_permlane32_swap_b32_e32 v223, v224
	v_cvt_pk_bf16_f32 v147, v147, v234
	v_permlane32_swap_b32_e32 v144, v146
	v_cvt_pk_bf16_f32 v234, v231, v233
	v_cvt_pk_bf16_f32 v235, v230, v232
	v_cvt_pk_bf16_f32 v236, v227, v229
	v_cvt_pk_bf16_f32 v237, v226, v228
	v_cvt_pk_bf16_f32 v226, v134, v135
	v_cvt_pk_bf16_f32 v227, v138, v139
	v_cvt_pk_bf16_f32 v228, v130, v131
	v_cvt_pk_bf16_f32 v229, v132, v133
	v_cvt_pk_bf16_f32 v230, v136, v137
	v_cvt_pk_bf16_f32 v231, v142, v143
	v_cvt_pk_bf16_f32 v232, v140, v141
	v_cvt_pk_bf16_f32 v233, v128, v129
	v_permlane32_swap_b32_e32 v145, v147
	v_permlane32_swap_b32_e32 v234, v236
	v_permlane32_swap_b32_e32 v235, v237
	v_permlane32_swap_b32_e32 v226, v228
	v_permlane32_swap_b32_e32 v227, v229
	v_permlane32_swap_b32_e32 v230, v232
	v_permlane32_swap_b32_e32 v231, v233
	s_add_i32 s8, s19, 3
	s_cmp_lt_u32 s8, 12
	s_cselect_b64 s[10:11], -1, 0
	s_and_b64 s[8:9], s[10:11], exec
	s_cselect_b32 s8, 0, -12
	s_cselect_b32 s9, s13, 0x4000
	s_add_i32 s8, s8, s19
	s_lshl_b32 s8, s8, 6
	s_add_i32 s8, s8, s9
	s_mulk_i32 s8, 0x2400
	s_add_i32 s21, s8, 0x1b0000
	s_add_u32 s8, s14, s21
	s_addc_u32 s9, s15, 0
	s_add_u32 vcc_lo, s16, s21
	s_addc_u32 vcc_hi, s17, 0
	v_lshl_add_u64 v[128:129], vcc, 0, v[192:193]
	v_lshl_add_u64 v[132:133], vcc, 0, v[150:151]
	v_lshl_add_u64 v[136:137], s[8:9], 0, v[192:193]
	v_lshl_add_u64 v[140:141], s[8:9], 0, v[150:151]
	global_load_dwordx4 v[128:131], v[128:129], off
	s_nop 0
	global_load_dwordx4 v[132:135], v[132:133], off
	s_nop 0
	global_load_dwordx4 v[136:139], v[136:137], off
	s_nop 0
	global_load_dwordx4 v[140:143], v[140:141], off
	s_cmp_gt_u32 s20, 11
	s_waitcnt lgkmcnt(3)
	v_mfma_f32_32x32x16_bf16 v[80:95], v[64:67], v[100:103], 0
	s_waitcnt lgkmcnt(2)
	v_mfma_f32_32x32x16_bf16 v[80:95], v[240:243], v[104:107], v[80:95]
	ds_read_b128 v[240:243], v162 offset:49152
	s_waitcnt lgkmcnt(2)
	v_mfma_f32_32x32x16_bf16 v[64:79], v[244:247], v[100:103], 0
	ds_read_b128 v[244:247], v162 offset:57344
	s_waitcnt lgkmcnt(2)
	v_mfma_f32_32x32x16_bf16 v[64:79], v[248:251], v[104:107], v[64:79]
	ds_read_b128 v[248:251], v160 offset:49152
	s_waitcnt lgkmcnt(2)
	v_mfma_f32_32x32x16_bf16 v[80:95], v[240:243], v[120:123], v[80:95]
	ds_read_b128 v[240:243], v160 offset:57344
	s_waitcnt lgkmcnt(2)
	v_mfma_f32_32x32x16_bf16 v[64:79], v[244:247], v[120:123], v[64:79]
	ds_read_b128 v[244:247], v166 offset:49152
	s_waitcnt lgkmcnt(2)
	v_mfma_f32_32x32x16_bf16 v[80:95], v[248:251], v[124:127], v[80:95]
	ds_read_b128 v[248:251], v166 offset:57344
	s_waitcnt lgkmcnt(2)
	v_mfma_f32_32x32x16_bf16 v[64:79], v[240:243], v[124:127], v[64:79]
	ds_read_b128 v[240:243], v165 offset:49152
	s_waitcnt lgkmcnt(2)
	v_mfma_f32_32x32x16_bf16 v[80:95], v[244:247], v[116:119], v[80:95]
	ds_read_b128 v[244:247], v165 offset:57344
	s_waitcnt lgkmcnt(2)
	v_mfma_f32_32x32x16_bf16 v[64:79], v[248:251], v[116:119], v[64:79]
	ds_read_b128 v[248:251], v164 offset:49152
	s_waitcnt lgkmcnt(2)
	v_mfma_f32_32x32x16_bf16 v[80:95], v[240:243], v[112:115], v[80:95]
	ds_read_b128 v[240:243], v164 offset:57344
	s_waitcnt lgkmcnt(2)
	v_mfma_f32_32x32x16_bf16 v[64:79], v[244:247], v[112:115], v[64:79]
	ds_read_b128 v[244:247], v163 offset:49152
	s_waitcnt lgkmcnt(2)
	v_mfma_f32_32x32x16_bf16 v[80:95], v[248:251], v[108:111], v[80:95]
	ds_read_b128 v[248:251], v163 offset:57344
	s_waitcnt lgkmcnt(2)
	v_mfma_f32_32x32x16_bf16 v[64:79], v[240:243], v[108:111], v[64:79]
	s_waitcnt lgkmcnt(1)
	v_mfma_f32_32x32x16_bf16 v[80:95], v[244:247], v[96:99], v[80:95]
	s_waitcnt lgkmcnt(0)
	v_mfma_f32_32x32x16_bf16 v[64:79], v[248:251], v[96:99], v[64:79]
	s_cbranch_scc1 .LBB0_612
	v_add3_u32 v219, v215, s19, 2
	v_max_i32_e32 v219, -7, v219
	v_add_u32_e32 v219, 7, v219
	s_add_i32 s8, s12, s19
	v_min_u32_e32 v219, 14, v219
	s_add_i32 s8, s8, 2
	v_mul_u32_u24_e32 v219, 31, v219
	v_cmp_ge_u32_e32 vcc, s8, v169
	v_cmp_lt_u32_e64 s[8:9], s8, v170
	v_sub_u32_e32 v219, v219, v168
	s_and_b64 s[8:9], vcc, s[8:9]
	v_add_u32_e32 v219, 15, v219
	v_mov_b32_e32 v218, 0x1d1
	v_add_u32_e32 v239, v219, v173
	s_and_b64 vcc, s[36:37], s[8:9]
	v_cndmask_b32_e32 v239, v218, v239, vcc
	v_lshl_add_u32 v239, v239, 2, s18
	ds_read_b32 v239, v239
	v_readlane_b32 s10, v255, 28
	v_readlane_b32 s11, v255, 29
	v_readlane_b32 s22, v255, 30
	s_and_b64 s[10:11], s[8:9], s[10:11]
	v_add_u32_e32 v240, v219, v174
	s_and_b64 vcc, s[38:39], s[8:9]
	v_cndmask_b32_e32 v240, v218, v240, vcc
	v_lshl_add_u32 v240, v240, 2, s18
	ds_read_b32 v240, v240
	v_readlane_b32 s23, v255, 31
	v_add_u32_e32 v241, v219, v175
	s_and_b64 vcc, s[40:41], s[8:9]
	v_cndmask_b32_e32 v241, v218, v241, vcc
	v_lshl_add_u32 v241, v241, 2, s18
	ds_read_b32 v241, v241
	v_add_u32_e32 v242, v219, v176
	s_and_b64 vcc, s[42:43], s[8:9]
	v_cndmask_b32_e32 v242, v218, v242, vcc
	v_lshl_add_u32 v242, v242, 2, s18
	ds_read_b32 v242, v242
	v_add_u32_e32 v243, v219, v177
	s_and_b64 vcc, s[8:9], s[44:45]
	v_cndmask_b32_e32 v243, v218, v243, vcc
	v_lshl_add_u32 v243, v243, 2, s18
	ds_read_b32 v243, v243
	v_add_u32_e32 v244, v219, v178
	s_and_b64 vcc, s[8:9], s[46:47]
	v_cndmask_b32_e32 v244, v218, v244, vcc
	v_lshl_add_u32 v244, v244, 2, s18
	ds_read_b32 v244, v244
	v_add_u32_e32 v245, v219, v179
	s_and_b64 vcc, s[8:9], s[48:49]
	v_cndmask_b32_e32 v245, v218, v245, vcc
	v_lshl_add_u32 v245, v245, 2, s18
	ds_read_b32 v245, v245
	v_add_u32_e32 v246, v219, v180
	s_and_b64 vcc, s[8:9], s[50:51]
	v_cndmask_b32_e32 v246, v218, v246, vcc
	v_lshl_add_u32 v246, v246, 2, s18
	ds_read_b32 v246, v246
	v_add_u32_e32 v247, v219, v181
	s_and_b64 vcc, s[10:11], s[22:23]
	v_cndmask_b32_e32 v247, v218, v247, vcc
	v_lshl_add_u32 v247, v247, 2, s18
	ds_read_b32 v247, v247
	v_readlane_b32 s10, v255, 32
	v_readlane_b32 s11, v255, 33
	v_readlane_b32 s22, v255, 34
	s_and_b64 s[10:11], s[8:9], s[10:11]
	v_readlane_b32 s23, v255, 35
	v_add_u32_e32 v248, v219, v182
	s_and_b64 vcc, s[10:11], s[22:23]
	v_cndmask_b32_e32 v248, v218, v248, vcc
	v_lshl_add_u32 v248, v248, 2, s18
	ds_read_b32 v248, v248
	v_readlane_b32 s10, v255, 36
	v_readlane_b32 s11, v255, 37
	v_readlane_b32 s22, v255, 38
	s_and_b64 s[10:11], s[8:9], s[10:11]
	v_readlane_b32 s23, v255, 39
	v_add_u32_e32 v249, v219, v183
	s_and_b64 vcc, s[10:11], s[22:23]
	v_cndmask_b32_e32 v249, v218, v249, vcc
	v_lshl_add_u32 v249, v249, 2, s18
	ds_read_b32 v249, v249
	v_readlane_b32 s10, v255, 40
	v_readlane_b32 s11, v255, 41
	v_readlane_b32 s22, v255, 42
	s_and_b64 s[10:11], s[8:9], s[10:11]
	v_readlane_b32 s23, v255, 43
	v_add_u32_e32 v250, v219, v184
	s_and_b64 vcc, s[10:11], s[22:23]
	v_cndmask_b32_e32 v250, v218, v250, vcc
	v_lshl_add_u32 v250, v250, 2, s18
	ds_read_b32 v250, v250
	v_readlane_b32 s10, v255, 44
	v_readlane_b32 s11, v255, 45
	s_and_b64 s[10:11], s[8:9], s[10:11]
	v_add_u32_e32 v251, v219, v185
	s_and_b64 vcc, s[10:11], s[30:31]
	v_cndmask_b32_e32 v251, v218, v251, vcc
	v_lshl_add_u32 v251, v251, 2, s18
	ds_read_b32 v251, v251
	s_and_b64 s[10:11], s[8:9], s[34:35]
	v_add_u32_e32 v252, v219, v186
	s_and_b64 vcc, s[10:11], s[24:25]
	v_cndmask_b32_e32 v252, v218, v252, vcc
	v_lshl_add_u32 v252, v252, 2, s18
	ds_read_b32 v252, v252
	s_and_b64 s[10:11], s[8:9], s[26:27]
	v_add_u32_e32 v253, v219, v187
	s_and_b64 vcc, s[10:11], s[28:29]
	v_cndmask_b32_e32 v253, v218, v253, vcc
	v_lshl_add_u32 v253, v253, 2, s18
	ds_read_b32 v253, v253
	s_and_b64 s[10:11], s[8:9], s[52:53]
	s_waitcnt lgkmcnt(14)
	v_add_f32_e32 v80, v80, v239
	v_add_u32_e32 v239, v219, v188
	s_and_b64 vcc, s[10:11], s[54:55]
	v_cndmask_b32_e32 v239, v218, v239, vcc
	v_lshl_add_u32 v239, v239, 2, s18
	ds_read_b32 v239, v239
	s_and_b64 s[10:11], s[8:9], s[56:57]
	s_waitcnt lgkmcnt(14)
	v_add_f32_e32 v81, v81, v240
	v_add_u32_e32 v240, v219, v189
	s_and_b64 vcc, s[10:11], s[58:59]
	v_cndmask_b32_e32 v240, v218, v240, vcc
	v_lshl_add_u32 v240, v240, 2, s18
	ds_read_b32 v240, v240
	s_and_b64 s[10:11], s[8:9], s[60:61]
	s_waitcnt lgkmcnt(14)
	v_add_f32_e32 v82, v82, v241
	v_add_u32_e32 v241, v219, v190
	s_and_b64 vcc, s[10:11], s[62:63]
	v_cndmask_b32_e32 v241, v218, v241, vcc
	v_lshl_add_u32 v241, v241, 2, s18
	ds_read_b32 v241, v241
	s_and_b64 s[10:11], s[8:9], s[64:65]
	s_waitcnt lgkmcnt(14)
	v_add_f32_e32 v83, v83, v242
	v_add_u32_e32 v242, v219, v191
	s_and_b64 vcc, s[10:11], s[66:67]
	v_cndmask_b32_e32 v242, v218, v242, vcc
	v_lshl_add_u32 v242, v242, 2, s18
	ds_read_b32 v242, v242
	s_and_b64 s[10:11], s[8:9], s[68:69]
	s_waitcnt lgkmcnt(14)
	v_add_f32_e32 v84, v84, v243
	v_add_u32_e32 v243, v219, v200
	s_and_b64 vcc, s[10:11], s[70:71]
	v_cndmask_b32_e32 v243, v218, v243, vcc
	v_lshl_add_u32 v243, v243, 2, s18
	ds_read_b32 v243, v243
	s_and_b64 s[10:11], s[8:9], s[72:73]
	s_waitcnt lgkmcnt(14)
	v_add_f32_e32 v85, v85, v244
	v_add_u32_e32 v244, v219, v201
	s_and_b64 vcc, s[10:11], s[74:75]
	v_cndmask_b32_e32 v244, v218, v244, vcc
	v_lshl_add_u32 v244, v244, 2, s18
	ds_read_b32 v244, v244
	s_and_b64 s[10:11], s[8:9], s[76:77]
	s_waitcnt lgkmcnt(14)
	v_add_f32_e32 v86, v86, v245
	v_add_u32_e32 v245, v219, v203
	s_and_b64 vcc, s[10:11], s[78:79]
	v_cndmask_b32_e32 v245, v218, v245, vcc
	v_lshl_add_u32 v245, v245, 2, s18
	ds_read_b32 v245, v245
	s_and_b64 s[10:11], s[8:9], s[80:81]
	s_waitcnt lgkmcnt(14)
	v_add_f32_e32 v87, v87, v246
	v_add_u32_e32 v246, v219, v204
	s_and_b64 vcc, s[10:11], s[82:83]
	v_cndmask_b32_e32 v246, v218, v246, vcc
	v_lshl_add_u32 v246, v246, 2, s18
	ds_read_b32 v246, v246
	s_and_b64 s[10:11], s[8:9], s[84:85]
	s_waitcnt lgkmcnt(14)
	v_add_f32_e32 v88, v88, v247
	v_add_u32_e32 v247, v219, v205
	s_and_b64 vcc, s[10:11], s[86:87]
	v_cndmask_b32_e32 v247, v218, v247, vcc
	v_lshl_add_u32 v247, v247, 2, s18
	ds_read_b32 v247, v247
	s_waitcnt lgkmcnt(14)
	v_add_f32_e32 v89, v89, v248
	v_add_u32_e32 v248, v219, v206
	s_and_b64 vcc, s[8:9], s[88:89]
	v_cndmask_b32_e32 v248, v218, v248, vcc
	v_lshl_add_u32 v248, v248, 2, s18
	ds_read_b32 v248, v248
	s_waitcnt lgkmcnt(14)
	v_add_f32_e32 v90, v90, v249
	v_add_u32_e32 v249, v219, v207
	s_and_b64 vcc, s[8:9], s[90:91]
	v_cndmask_b32_e32 v249, v218, v249, vcc
	v_lshl_add_u32 v249, v249, 2, s18
	ds_read_b32 v249, v249
	s_waitcnt lgkmcnt(14)
	v_add_f32_e32 v91, v91, v250
	v_add_u32_e32 v250, v219, v208
	s_and_b64 vcc, s[8:9], s[92:93]
	v_cndmask_b32_e32 v250, v218, v250, vcc
	v_lshl_add_u32 v250, v250, 2, s18
	ds_read_b32 v250, v250
	s_waitcnt lgkmcnt(14)
	v_add_f32_e32 v92, v92, v251
	v_add_u32_e32 v251, v219, v209
	s_and_b64 vcc, s[8:9], s[94:95]
	v_cndmask_b32_e32 v251, v218, v251, vcc
	v_lshl_add_u32 v251, v251, 2, s18
	ds_read_b32 v251, v251
	s_waitcnt lgkmcnt(14)
	v_add_f32_e32 v93, v93, v252
	v_add_u32_e32 v252, v219, v210
	s_and_b64 vcc, s[8:9], s[96:97]
	v_cndmask_b32_e32 v252, v218, v252, vcc
	v_lshl_add_u32 v252, v252, 2, s18
	ds_read_b32 v252, v252
	s_waitcnt lgkmcnt(14)
	v_add_f32_e32 v94, v94, v253
	v_add_u32_e32 v253, v219, v211
	s_and_b64 vcc, s[8:9], s[2:3]
	v_cndmask_b32_e32 v253, v218, v253, vcc
	v_lshl_add_u32 v253, v253, 2, s18
	ds_read_b32 v253, v253
	s_waitcnt lgkmcnt(14)
	v_add_f32_e32 v95, v95, v239
	v_add_u32_e32 v239, v219, v212
	s_and_b64 vcc, s[8:9], s[0:1]
	v_cndmask_b32_e32 v239, v218, v239, vcc
	v_lshl_add_u32 v239, v239, 2, s18
	ds_read_b32 v239, v239
	s_waitcnt lgkmcnt(14)
	v_add_f32_e32 v64, v64, v240
	v_add_u32_e32 v240, v219, v213
	s_and_b64 vcc, s[8:9], s[6:7]
	v_cndmask_b32_e32 v240, v218, v240, vcc
	v_lshl_add_u32 v240, v240, 2, s18
	ds_read_b32 v240, v240
	s_waitcnt lgkmcnt(14)
	v_add_f32_e32 v65, v65, v241
	s_waitcnt lgkmcnt(13)
	v_add_f32_e32 v66, v66, v242
	s_waitcnt lgkmcnt(12)
	v_add_f32_e32 v67, v67, v243
	s_waitcnt lgkmcnt(11)
	v_add_f32_e32 v68, v68, v244
	s_waitcnt lgkmcnt(10)
	v_add_f32_e32 v69, v69, v245
	s_waitcnt lgkmcnt(9)
	v_add_f32_e32 v70, v70, v246
	s_waitcnt lgkmcnt(8)
	v_add_f32_e32 v71, v71, v247
	s_waitcnt lgkmcnt(7)
	v_add_f32_e32 v72, v72, v248
	s_waitcnt lgkmcnt(6)
	v_add_f32_e32 v73, v73, v249
	s_waitcnt lgkmcnt(5)
	v_add_f32_e32 v74, v74, v250
	s_waitcnt lgkmcnt(4)
	v_add_f32_e32 v75, v75, v251
	s_waitcnt lgkmcnt(3)
	v_add_f32_e32 v76, v76, v252
	s_waitcnt lgkmcnt(2)
	v_add_f32_e32 v77, v77, v253
	s_waitcnt lgkmcnt(1)
	v_add_f32_e32 v78, v78, v239
	s_waitcnt lgkmcnt(0)
	v_add_f32_e32 v79, v79, v240
.LBB0_612:
	s_add_i32 s8, s19, 3
	s_cmp_lt_u32 s8, 12
	s_cselect_b64 s[10:11], -1, 0
	ds_read_b64_tr_b16 v[238:239], v202 offset:0
	ds_read_b64_tr_b16 v[240:241], v202 offset:0x800
	ds_read_b64_tr_b16 v[242:243], v202 offset:0x1000
	ds_read_b64_tr_b16 v[244:245], v202 offset:0x1800
	ds_read_b64_tr_b16 v[246:247], v202 offset:0x2000
	ds_read_b64_tr_b16 v[248:249], v202 offset:0x2800
	ds_read_b64_tr_b16 v[250:251], v202 offset:0x3000
	ds_read_b64_tr_b16 v[252:253], v202 offset:0x3800
	s_waitcnt lgkmcnt(0)
	s_nop 0
	v_mfma_f32_32x32x16_bf16 v[0:15], v[144:147], v[238:241], v[0:15]
	ds_read_b64_tr_b16 v[238:239], v202 offset:0x200
	ds_read_b64_tr_b16 v[240:241], v202 offset:0xa00
	v_mfma_f32_32x32x16_bf16 v[0:15], v[234:237], v[242:245], v[0:15]
	ds_read_b64_tr_b16 v[242:243], v202 offset:0x1200
	ds_read_b64_tr_b16 v[244:245], v202 offset:0x1a00
	v_mfma_f32_32x32x16_bf16 v[0:15], v[226:229], v[246:249], v[0:15]
	ds_read_b64_tr_b16 v[246:247], v202 offset:0x2200
	ds_read_b64_tr_b16 v[248:249], v202 offset:0x2a00
	v_mfma_f32_32x32x16_bf16 v[0:15], v[230:233], v[250:253], v[0:15]
	ds_read_b64_tr_b16 v[250:251], v202 offset:0x3200
	ds_read_b64_tr_b16 v[252:253], v202 offset:0x3a00
	s_waitcnt lgkmcnt(0)
	v_mfma_f32_32x32x16_bf16 v[48:63], v[144:147], v[238:241], v[48:63]
	ds_read_b64_tr_b16 v[238:239], v202 offset:0x400
	ds_read_b64_tr_b16 v[240:241], v202 offset:0xc00
	v_mfma_f32_32x32x16_bf16 v[48:63], v[234:237], v[242:245], v[48:63]
	ds_read_b64_tr_b16 v[242:243], v202 offset:0x1400
	ds_read_b64_tr_b16 v[244:245], v202 offset:0x1c00
	v_mfma_f32_32x32x16_bf16 v[48:63], v[226:229], v[246:249], v[48:63]
	ds_read_b64_tr_b16 v[246:247], v202 offset:0x2400
	ds_read_b64_tr_b16 v[248:249], v202 offset:0x2c00
	v_mfma_f32_32x32x16_bf16 v[48:63], v[230:233], v[250:253], v[48:63]
	ds_read_b64_tr_b16 v[250:251], v202 offset:0x3400
	ds_read_b64_tr_b16 v[252:253], v202 offset:0x3c00
	s_waitcnt lgkmcnt(0)
	v_mfma_f32_32x32x16_bf16 v[32:47], v[144:147], v[238:241], v[32:47]
	ds_read_b64_tr_b16 v[238:239], v202 offset:0x600
	ds_read_b64_tr_b16 v[240:241], v202 offset:0xe00
	v_mfma_f32_32x32x16_bf16 v[32:47], v[234:237], v[242:245], v[32:47]
	ds_read_b64_tr_b16 v[242:243], v202 offset:0x1600
	ds_read_b64_tr_b16 v[244:245], v202 offset:0x1e00
	v_mfma_f32_32x32x16_bf16 v[32:47], v[226:229], v[246:249], v[32:47]
	ds_read_b64_tr_b16 v[246:247], v202 offset:0x2600
	ds_read_b64_tr_b16 v[248:249], v202 offset:0x2e00
	v_mfma_f32_32x32x16_bf16 v[32:47], v[230:233], v[250:253], v[32:47]
	ds_read_b64_tr_b16 v[250:251], v202 offset:0x3600
	ds_read_b64_tr_b16 v[252:253], v202 offset:0x3e00
	s_waitcnt lgkmcnt(0)
	v_mfma_f32_32x32x16_bf16 v[16:31], v[144:147], v[238:241], v[16:31]
	v_max_f32_e32 v144, v81, v81
	v_max_f32_e32 v145, v80, v80
	v_max_f32_e32 v144, v145, v144
	v_max3_f32 v144, v144, v82, v83
	v_max3_f32 v144, v144, v84, v85
	v_max3_f32 v144, v144, v86, v87
	v_max3_f32 v144, v144, v88, v89
	v_max3_f32 v144, v144, v90, v91
	v_max3_f32 v144, v144, v92, v93
	v_mfma_f32_32x32x16_bf16 v[16:31], v[234:237], v[242:245], v[16:31]
	v_max3_f32 v144, v144, v94, v95
	v_max3_f32 v144, v144, v64, v65
	v_max3_f32 v144, v144, v66, v67
	v_max3_f32 v144, v144, v68, v69
	v_max3_f32 v144, v144, v70, v71
	v_max3_f32 v144, v144, v72, v73
	v_max3_f32 v144, v144, v74, v75
	v_max3_f32 v144, v144, v76, v77
	v_mfma_f32_32x32x16_bf16 v[16:31], v[226:229], v[246:249], v[16:31]
	v_max3_f32 v144, v144, v78, v79
	v_mov_b32_e32 v145, v144
	s_nop 1
	v_permlane32_swap_b32_e32 v144, v145
	v_max_f32_e32 v145, v145, v145
	v_max_f32_e32 v144, v144, v144
	v_max_f32_e32 v144, v144, v145
	v_sub_f32_e32 v145, v144, v222
	s_mov_b32 s8, 0x42b504f3
	v_cmp_ge_f32_e32 vcc, s8, v145
	v_max_f32_e32 v145, v222, v222
	v_max_f32_e32 v144, v145, v144
	v_mfma_f32_32x32x16_bf16 v[16:31], v[230:233], v[250:253], v[16:31]
	v_sub_f32_e32 v145, v222, v144
	v_mul_f32_e32 v145, 0x3e0293ee, v145
	v_exp_f32_e32 v145, v145
	s_cmp_eq_u64 vcc, exec
	s_cselect_b64 s[8:9], -1, 0
	s_barrier
	s_waitcnt vmcnt(0)
	v_cndmask_b32_e64 v225, v145, 1.0, s[8:9]
	v_cmp_gt_f32_e32 vcc, 1.0, v225
	s_waitcnt vmcnt(3)
	ds_write_b128 v156, v[128:131]
	s_waitcnt vmcnt(2)
	ds_write_b128 v157, v[132:135]
	s_waitcnt vmcnt(1)
	ds_write_b128 v153, v[136:139] offset:32768
	s_waitcnt vmcnt(0)
	ds_write_b128 v155, v[140:143] offset:32768
	s_cbranch_vccz .LBB0_616
	s_and_saveexec_b64 vcc, s[4:5]
	ds_write_b32 v171, v225 offset:128
	s_or_b64 exec, exec, vcc
	s_waitcnt lgkmcnt(0)
	v_add_u32_e32 v140, v159, v148
	ds_read_b128 v[128:131], v140 offset:224
	ds_read_b128 v[132:135], v140 offset:192
	ds_read_b128 v[136:139], v140 offset:160
	ds_read_b128 v[140:143], v140 offset:128
	s_waitcnt lgkmcnt(3)
	v_pk_mul_f32 v[12:13], v[12:13], v[128:129]
	s_waitcnt lgkmcnt(2)
	v_pk_mul_f32 v[8:9], v[8:9], v[132:133]
	s_waitcnt lgkmcnt(1)
	v_pk_mul_f32 v[4:5], v[4:5], v[136:137]
	v_pk_mul_f32 v[14:15], v[14:15], v[130:131]
	v_pk_mul_f32 v[10:11], v[10:11], v[134:135]
	v_pk_mul_f32 v[6:7], v[6:7], v[138:139]
	s_waitcnt lgkmcnt(0)
	v_pk_mul_f32 v[2:3], v[2:3], v[142:143]
	v_pk_mul_f32 v[0:1], v[0:1], v[140:141]
	v_pk_mul_f32 v[60:61], v[60:61], v[128:129]
	v_pk_mul_f32 v[56:57], v[56:57], v[132:133]
	v_pk_mul_f32 v[52:53], v[52:53], v[136:137]
	v_pk_mul_f32 v[62:63], v[62:63], v[130:131]
	v_pk_mul_f32 v[58:59], v[58:59], v[134:135]
	v_pk_mul_f32 v[54:55], v[54:55], v[138:139]
	v_pk_mul_f32 v[50:51], v[50:51], v[142:143]
	v_pk_mul_f32 v[48:49], v[48:49], v[140:141]
	v_pk_mul_f32 v[44:45], v[44:45], v[128:129]
	v_pk_mul_f32 v[40:41], v[40:41], v[132:133]
	v_pk_mul_f32 v[36:37], v[36:37], v[136:137]
	v_pk_mul_f32 v[46:47], v[46:47], v[130:131]
	v_pk_mul_f32 v[42:43], v[42:43], v[134:135]
	v_pk_mul_f32 v[38:39], v[38:39], v[138:139]
	v_pk_mul_f32 v[34:35], v[34:35], v[142:143]
	v_pk_mul_f32 v[32:33], v[32:33], v[140:141]
	v_pk_mul_f32 v[28:29], v[28:29], v[128:129]
	v_pk_mul_f32 v[24:25], v[24:25], v[132:133]
	v_pk_mul_f32 v[20:21], v[20:21], v[136:137]
	v_pk_mul_f32 v[30:31], v[30:31], v[130:131]
	v_pk_mul_f32 v[26:27], v[26:27], v[134:135]
	v_pk_mul_f32 v[22:23], v[22:23], v[138:139]
	v_pk_mul_f32 v[18:19], v[18:19], v[142:143]
	v_pk_mul_f32 v[16:17], v[16:17], v[140:141]
.LBB0_616:
	v_cndmask_b32_e64 v222, v144, v222, s[8:9]
	v_mul_f32_e32 v144, 0xbe0293ee, v222
	v_fmamk_f32 v80, v80, 0x3e0293ee, v144
	v_fmamk_f32 v81, v81, 0x3e0293ee, v144
	v_fmamk_f32 v82, v82, 0x3e0293ee, v144
	v_fmamk_f32 v83, v83, 0x3e0293ee, v144
	v_fmamk_f32 v84, v84, 0x3e0293ee, v144
	v_fmamk_f32 v85, v85, 0x3e0293ee, v144
	v_fmamk_f32 v86, v86, 0x3e0293ee, v144
	v_fmamk_f32 v87, v87, 0x3e0293ee, v144
	v_fmamk_f32 v88, v88, 0x3e0293ee, v144
	v_fmamk_f32 v89, v89, 0x3e0293ee, v144
	v_fmamk_f32 v90, v90, 0x3e0293ee, v144
	v_fmamk_f32 v91, v91, 0x3e0293ee, v144
	v_fmamk_f32 v92, v92, 0x3e0293ee, v144
	v_fmamk_f32 v93, v93, 0x3e0293ee, v144
	v_fmamk_f32 v94, v94, 0x3e0293ee, v144
	v_fmamk_f32 v95, v95, 0x3e0293ee, v144
	v_exp_f32_e32 v141, v80
	v_exp_f32_e32 v143, v81
	v_exp_f32_e32 v139, v82
	v_exp_f32_e32 v142, v83
	v_exp_f32_e32 v137, v84
	v_exp_f32_e32 v140, v85
	v_exp_f32_e32 v136, v86
	v_exp_f32_e32 v138, v87
	v_exp_f32_e32 v133, v88
	v_exp_f32_e32 v135, v89
	v_exp_f32_e32 v131, v90
	v_exp_f32_e32 v134, v91
	v_exp_f32_e32 v129, v92
	v_exp_f32_e32 v132, v93
	v_exp_f32_e32 v128, v94
	v_exp_f32_e32 v130, v95
	v_fmamk_f32 v145, v64, 0x3e0293ee, v144
	v_fmamk_f32 v146, v65, 0x3e0293ee, v144
	v_fmamk_f32 v147, v66, 0x3e0293ee, v144
	v_fmamk_f32 v226, v67, 0x3e0293ee, v144
	v_fmamk_f32 v227, v68, 0x3e0293ee, v144
	v_fmamk_f32 v228, v69, 0x3e0293ee, v144
	v_fmamk_f32 v229, v70, 0x3e0293ee, v144
	v_fmamk_f32 v230, v71, 0x3e0293ee, v144
	v_fmamk_f32 v231, v72, 0x3e0293ee, v144
	v_fmamk_f32 v232, v73, 0x3e0293ee, v144
	v_fmamk_f32 v233, v74, 0x3e0293ee, v144
	v_fmamk_f32 v234, v75, 0x3e0293ee, v144
	v_fmamk_f32 v235, v76, 0x3e0293ee, v144
	v_fmamk_f32 v236, v77, 0x3e0293ee, v144
	v_fmamk_f32 v237, v78, 0x3e0293ee, v144
	v_fmac_f32_e32 v144, 0x3e0293ee, v79
	s_waitcnt lgkmcnt(0)
	s_barrier
	ds_read_b128 v[64:67], v158 offset:32768
	ds_read_b128 v[250:253], v161 offset:32768
	s_andn2_b64 vcc, exec, s[10:11]
	v_exp_f32_e32 v249, v144
	v_add_f32_e32 v144, 0, v141
	v_add_f32_e32 v144, v143, v144
	v_add_f32_e32 v144, v139, v144
	v_add_f32_e32 v144, v142, v144
	v_add_f32_e32 v144, v137, v144
	v_add_f32_e32 v144, v140, v144
	v_add_f32_e32 v144, v136, v144
	v_add_f32_e32 v144, v138, v144
	v_add_f32_e32 v144, v133, v144
	v_add_f32_e32 v144, v135, v144
	v_add_f32_e32 v144, v131, v144
	v_add_f32_e32 v144, v134, v144
	v_exp_f32_e32 v218, v145
	v_add_f32_e32 v144, v129, v144
	v_exp_f32_e32 v219, v146
	v_add_f32_e32 v144, v132, v144
	v_exp_f32_e32 v220, v147
	v_add_f32_e32 v144, v128, v144
	v_exp_f32_e32 v221, v226
	v_add_f32_e32 v144, v130, v144
	v_exp_f32_e32 v238, v227
	v_add_f32_e32 v144, v218, v144
	v_exp_f32_e32 v241, v228
	v_add_f32_e32 v144, v219, v144
	v_exp_f32_e32 v242, v229
	v_add_f32_e32 v144, v220, v144
	v_exp_f32_e32 v243, v230
	v_add_f32_e32 v144, v221, v144
	v_exp_f32_e32 v244, v231
	v_add_f32_e32 v144, v238, v144
	v_exp_f32_e32 v245, v232
	v_add_f32_e32 v144, v241, v144
	v_exp_f32_e32 v246, v233
	v_add_f32_e32 v144, v242, v144
	v_exp_f32_e32 v247, v234
	v_add_f32_e32 v144, v243, v144
	v_exp_f32_e32 v248, v235
	v_add_f32_e32 v144, v244, v144
	v_exp_f32_e32 v236, v236
	v_add_f32_e32 v144, v245, v144
	v_exp_f32_e32 v237, v237
	v_add_f32_e32 v144, v246, v144
	v_add_f32_e32 v144, v247, v144
	v_add_f32_e32 v144, v248, v144
	v_add_f32_e32 v144, v236, v144
	v_add_f32_e32 v144, v237, v144
	v_add_f32_e32 v239, v249, v144
	v_mov_b32_e32 v240, v239
	v_cvt_pk_bf16_f32 v144, v141, v143
	v_cvt_pk_bf16_f32 v145, v139, v142
	v_cvt_pk_bf16_f32 v146, v137, v140
	v_cvt_pk_bf16_f32 v147, v136, v138
	s_nop 1
	v_permlane32_swap_b32_e32 v239, v240
	v_permlane32_swap_b32_e32 v144, v146
	v_permlane32_swap_b32_e32 v145, v147
	v_cvt_pk_bf16_f32 v226, v133, v135
	v_cvt_pk_bf16_f32 v227, v131, v134
	v_cvt_pk_bf16_f32 v228, v129, v132
	v_cvt_pk_bf16_f32 v229, v128, v130
	v_cvt_pk_bf16_f32 v230, v218, v219
	v_cvt_pk_bf16_f32 v231, v220, v221
	v_cvt_pk_bf16_f32 v232, v238, v241
	v_cvt_pk_bf16_f32 v233, v242, v243
	v_cvt_pk_bf16_f32 v234, v244, v245
	v_cvt_pk_bf16_f32 v235, v246, v247
	v_cvt_pk_bf16_f32 v236, v248, v236
	v_cvt_pk_bf16_f32 v237, v237, v249
	s_nop 0
	v_permlane32_swap_b32_e32 v226, v228
	v_permlane32_swap_b32_e32 v227, v229
	v_permlane32_swap_b32_e32 v230, v232
	v_permlane32_swap_b32_e32 v231, v233
	v_permlane32_swap_b32_e32 v234, v236
	v_permlane32_swap_b32_e32 v235, v237
	ds_read_b128 v[242:245], v158 offset:40960
	ds_read_b128 v[246:249], v161 offset:40960
	s_cmp_lt_u32 s20, 10
	s_cselect_b32 s8, 0, -12
	s_cselect_b32 s9, s13, 0x4000
	s_add_i32 s8, s8, s19
	s_lshl_b32 s8, s8, 6
	s_add_i32 s8, s8, s9
	s_mulk_i32 s8, 0x2400
	s_add_i32 s10, s8, 0x240000
	s_add_u32 s8, s14, s10
	s_addc_u32 s9, s15, 0
	s_add_u32 s10, s16, s10
	s_addc_u32 s11, s17, 0
	v_lshl_add_u64 v[128:129], s[10:11], 0, v[192:193]
	v_lshl_add_u64 v[132:133], s[10:11], 0, v[150:151]
	v_lshl_add_u64 v[136:137], s[8:9], 0, v[192:193]
	v_lshl_add_u64 v[140:141], s[8:9], 0, v[150:151]
	global_load_dwordx4 v[128:131], v[128:129], off
	s_nop 0
	global_load_dwordx4 v[132:135], v[132:133], off
	s_nop 0
	global_load_dwordx4 v[136:139], v[136:137], off
	s_nop 0
	global_load_dwordx4 v[140:143], v[140:141], off
	s_waitcnt lgkmcnt(3)
	v_mfma_f32_32x32x16_bf16 v[80:95], v[64:67], v[100:103], 0
	s_waitcnt lgkmcnt(2)
	v_mfma_f32_32x32x16_bf16 v[80:95], v[250:253], v[104:107], v[80:95]
	ds_read_b128 v[250:253], v162 offset:32768
	s_waitcnt lgkmcnt(2)
	v_mfma_f32_32x32x16_bf16 v[64:79], v[242:245], v[100:103], 0
	ds_read_b128 v[242:245], v162 offset:40960
	s_waitcnt lgkmcnt(2)
	v_mfma_f32_32x32x16_bf16 v[64:79], v[246:249], v[104:107], v[64:79]
	ds_read_b128 v[246:249], v160 offset:32768
	s_waitcnt lgkmcnt(2)
	v_mfma_f32_32x32x16_bf16 v[80:95], v[250:253], v[120:123], v[80:95]
	ds_read_b128 v[250:253], v160 offset:40960
	s_waitcnt lgkmcnt(2)
	v_mfma_f32_32x32x16_bf16 v[64:79], v[242:245], v[120:123], v[64:79]
	ds_read_b128 v[242:245], v166 offset:32768
	s_waitcnt lgkmcnt(2)
	v_mfma_f32_32x32x16_bf16 v[80:95], v[246:249], v[124:127], v[80:95]
	ds_read_b128 v[246:249], v166 offset:40960
	s_waitcnt lgkmcnt(2)
	v_mfma_f32_32x32x16_bf16 v[64:79], v[250:253], v[124:127], v[64:79]
	ds_read_b128 v[250:253], v165 offset:32768
	s_waitcnt lgkmcnt(2)
	v_mfma_f32_32x32x16_bf16 v[80:95], v[242:245], v[116:119], v[80:95]
	ds_read_b128 v[242:245], v165 offset:40960
	s_waitcnt lgkmcnt(2)
	v_mfma_f32_32x32x16_bf16 v[64:79], v[246:249], v[116:119], v[64:79]
	ds_read_b128 v[246:249], v164 offset:32768
	s_waitcnt lgkmcnt(2)
	v_mfma_f32_32x32x16_bf16 v[80:95], v[250:253], v[112:115], v[80:95]
	ds_read_b128 v[250:253], v164 offset:40960
	s_waitcnt lgkmcnt(2)
	v_mfma_f32_32x32x16_bf16 v[64:79], v[242:245], v[112:115], v[64:79]
	ds_read_b128 v[242:245], v163 offset:32768
	s_waitcnt lgkmcnt(2)
	v_mfma_f32_32x32x16_bf16 v[80:95], v[246:249], v[108:111], v[80:95]
	ds_read_b128 v[246:249], v163 offset:40960
	s_waitcnt lgkmcnt(2)
	v_mfma_f32_32x32x16_bf16 v[64:79], v[250:253], v[108:111], v[64:79]
	s_waitcnt lgkmcnt(1)
	v_mfma_f32_32x32x16_bf16 v[80:95], v[242:245], v[96:99], v[80:95]
	s_waitcnt lgkmcnt(0)
	v_mfma_f32_32x32x16_bf16 v[64:79], v[246:249], v[96:99], v[64:79]
	s_cbranch_vccnz .LBB0_618
	v_add3_u32 v218, v215, s19, 3
	v_max_i32_e32 v218, -7, v218
	v_add_u32_e32 v218, 7, v218
	s_add_i32 s8, s12, s19
	v_min_u32_e32 v218, 14, v218
	s_add_i32 s8, s8, 3
	v_mul_u32_u24_e32 v218, 31, v218
	v_cmp_ge_u32_e32 vcc, s8, v169
	v_cmp_lt_u32_e64 s[8:9], s8, v170
	v_sub_u32_e32 v218, v218, v168
	s_and_b64 s[8:9], vcc, s[8:9]
	v_add_u32_e32 v219, 15, v218
	v_mov_b32_e32 v218, 0x1d1
	v_add_u32_e32 v220, v219, v173
	s_and_b64 vcc, s[36:37], s[8:9]
	v_cndmask_b32_e32 v220, v218, v220, vcc
	v_lshl_add_u32 v220, v220, 2, s18
	ds_read_b32 v220, v220
	v_readlane_b32 s10, v255, 28
	v_readlane_b32 s11, v255, 29
	v_readlane_b32 s22, v255, 30
	s_and_b64 s[10:11], s[8:9], s[10:11]
	v_add_u32_e32 v221, v219, v174
	s_and_b64 vcc, s[38:39], s[8:9]
	v_cndmask_b32_e32 v221, v218, v221, vcc
	v_lshl_add_u32 v221, v221, 2, s18
	ds_read_b32 v221, v221
	v_readlane_b32 s23, v255, 31
	v_add_u32_e32 v241, v219, v175
	s_and_b64 vcc, s[40:41], s[8:9]
	v_cndmask_b32_e32 v241, v218, v241, vcc
	v_lshl_add_u32 v241, v241, 2, s18
	ds_read_b32 v241, v241
	v_add_u32_e32 v242, v219, v176
	s_and_b64 vcc, s[42:43], s[8:9]
	v_cndmask_b32_e32 v242, v218, v242, vcc
	v_lshl_add_u32 v242, v242, 2, s18
	ds_read_b32 v242, v242
	v_add_u32_e32 v243, v219, v177
	s_and_b64 vcc, s[8:9], s[44:45]
	v_cndmask_b32_e32 v243, v218, v243, vcc
	v_lshl_add_u32 v243, v243, 2, s18
	ds_read_b32 v243, v243
	v_add_u32_e32 v244, v219, v178
	s_and_b64 vcc, s[8:9], s[46:47]
	v_cndmask_b32_e32 v244, v218, v244, vcc
	v_lshl_add_u32 v244, v244, 2, s18
	ds_read_b32 v244, v244
	v_add_u32_e32 v245, v219, v179
	s_and_b64 vcc, s[8:9], s[48:49]
	v_cndmask_b32_e32 v245, v218, v245, vcc
	v_lshl_add_u32 v245, v245, 2, s18
	ds_read_b32 v245, v245
	v_add_u32_e32 v246, v219, v180
	s_and_b64 vcc, s[8:9], s[50:51]
	v_cndmask_b32_e32 v246, v218, v246, vcc
	v_lshl_add_u32 v246, v246, 2, s18
	ds_read_b32 v246, v246
	v_add_u32_e32 v247, v219, v181
	s_and_b64 vcc, s[10:11], s[22:23]
	v_cndmask_b32_e32 v247, v218, v247, vcc
	v_lshl_add_u32 v247, v247, 2, s18
	ds_read_b32 v247, v247
	v_readlane_b32 s10, v255, 32
	v_readlane_b32 s11, v255, 33
	v_readlane_b32 s22, v255, 34
	s_and_b64 s[10:11], s[8:9], s[10:11]
	v_readlane_b32 s23, v255, 35
	v_add_u32_e32 v248, v219, v182
	s_and_b64 vcc, s[10:11], s[22:23]
	v_cndmask_b32_e32 v248, v218, v248, vcc
	v_lshl_add_u32 v248, v248, 2, s18
	ds_read_b32 v248, v248
	v_readlane_b32 s10, v255, 36
	v_readlane_b32 s11, v255, 37
	v_readlane_b32 s22, v255, 38
	s_and_b64 s[10:11], s[8:9], s[10:11]
	v_readlane_b32 s23, v255, 39
	v_add_u32_e32 v249, v219, v183
	s_and_b64 vcc, s[10:11], s[22:23]
	v_cndmask_b32_e32 v249, v218, v249, vcc
	v_lshl_add_u32 v249, v249, 2, s18
	ds_read_b32 v249, v249
	v_readlane_b32 s10, v255, 40
	v_readlane_b32 s11, v255, 41
	v_readlane_b32 s22, v255, 42
	s_and_b64 s[10:11], s[8:9], s[10:11]
	v_readlane_b32 s23, v255, 43
	v_add_u32_e32 v250, v219, v184
	s_and_b64 vcc, s[10:11], s[22:23]
	v_cndmask_b32_e32 v250, v218, v250, vcc
	v_lshl_add_u32 v250, v250, 2, s18
	ds_read_b32 v250, v250
	v_readlane_b32 s10, v255, 44
	v_readlane_b32 s11, v255, 45
	s_and_b64 s[10:11], s[8:9], s[10:11]
	v_add_u32_e32 v251, v219, v185
	s_and_b64 vcc, s[10:11], s[30:31]
	v_cndmask_b32_e32 v251, v218, v251, vcc
	v_lshl_add_u32 v251, v251, 2, s18
	ds_read_b32 v251, v251
	s_and_b64 s[10:11], s[8:9], s[34:35]
	v_add_u32_e32 v252, v219, v186
	s_and_b64 vcc, s[10:11], s[24:25]
	v_cndmask_b32_e32 v252, v218, v252, vcc
	v_lshl_add_u32 v252, v252, 2, s18
	ds_read_b32 v252, v252
	s_and_b64 s[10:11], s[8:9], s[26:27]
	v_add_u32_e32 v253, v219, v187
	s_and_b64 vcc, s[10:11], s[28:29]
	v_cndmask_b32_e32 v253, v218, v253, vcc
	v_lshl_add_u32 v253, v253, 2, s18
	ds_read_b32 v253, v253
	s_and_b64 s[10:11], s[8:9], s[52:53]
	s_waitcnt lgkmcnt(14)
	v_add_f32_e32 v80, v80, v220
	v_add_u32_e32 v220, v219, v188
	s_and_b64 vcc, s[10:11], s[54:55]
	v_cndmask_b32_e32 v220, v218, v220, vcc
	v_lshl_add_u32 v220, v220, 2, s18
	ds_read_b32 v220, v220
	s_and_b64 s[10:11], s[8:9], s[56:57]
	s_waitcnt lgkmcnt(14)
	v_add_f32_e32 v81, v81, v221
	v_add_u32_e32 v221, v219, v189
	s_and_b64 vcc, s[10:11], s[58:59]
	v_cndmask_b32_e32 v221, v218, v221, vcc
	v_lshl_add_u32 v221, v221, 2, s18
	ds_read_b32 v221, v221
	s_and_b64 s[10:11], s[8:9], s[60:61]
	s_waitcnt lgkmcnt(14)
	v_add_f32_e32 v82, v82, v241
	v_add_u32_e32 v241, v219, v190
	s_and_b64 vcc, s[10:11], s[62:63]
	v_cndmask_b32_e32 v241, v218, v241, vcc
	v_lshl_add_u32 v241, v241, 2, s18
	ds_read_b32 v241, v241
	s_and_b64 s[10:11], s[8:9], s[64:65]
	s_waitcnt lgkmcnt(14)
	v_add_f32_e32 v83, v83, v242
	v_add_u32_e32 v242, v219, v191
	s_and_b64 vcc, s[10:11], s[66:67]
	v_cndmask_b32_e32 v242, v218, v242, vcc
	v_lshl_add_u32 v242, v242, 2, s18
	ds_read_b32 v242, v242
	s_and_b64 s[10:11], s[8:9], s[68:69]
	s_waitcnt lgkmcnt(14)
	v_add_f32_e32 v84, v84, v243
	v_add_u32_e32 v243, v219, v200
	s_and_b64 vcc, s[10:11], s[70:71]
	v_cndmask_b32_e32 v243, v218, v243, vcc
	v_lshl_add_u32 v243, v243, 2, s18
	ds_read_b32 v243, v243
	s_and_b64 s[10:11], s[8:9], s[72:73]
	s_waitcnt lgkmcnt(14)
	v_add_f32_e32 v85, v85, v244
	v_add_u32_e32 v244, v219, v201
	s_and_b64 vcc, s[10:11], s[74:75]
	v_cndmask_b32_e32 v244, v218, v244, vcc
	v_lshl_add_u32 v244, v244, 2, s18
	ds_read_b32 v244, v244
	s_and_b64 s[10:11], s[8:9], s[76:77]
	s_waitcnt lgkmcnt(14)
	v_add_f32_e32 v86, v86, v245
	v_add_u32_e32 v245, v219, v203
	s_and_b64 vcc, s[10:11], s[78:79]
	v_cndmask_b32_e32 v245, v218, v245, vcc
	v_lshl_add_u32 v245, v245, 2, s18
	ds_read_b32 v245, v245
	s_and_b64 s[10:11], s[8:9], s[80:81]
	s_waitcnt lgkmcnt(14)
	v_add_f32_e32 v87, v87, v246
	v_add_u32_e32 v246, v219, v204
	s_and_b64 vcc, s[10:11], s[82:83]
	v_cndmask_b32_e32 v246, v218, v246, vcc
	v_lshl_add_u32 v246, v246, 2, s18
	ds_read_b32 v246, v246
	s_and_b64 s[10:11], s[8:9], s[84:85]
	s_waitcnt lgkmcnt(14)
	v_add_f32_e32 v88, v88, v247
	v_add_u32_e32 v247, v219, v205
	s_and_b64 vcc, s[10:11], s[86:87]
	v_cndmask_b32_e32 v247, v218, v247, vcc
	v_lshl_add_u32 v247, v247, 2, s18
	ds_read_b32 v247, v247
	s_waitcnt lgkmcnt(14)
	v_add_f32_e32 v89, v89, v248
	v_add_u32_e32 v248, v219, v206
	s_and_b64 vcc, s[8:9], s[88:89]
	v_cndmask_b32_e32 v248, v218, v248, vcc
	v_lshl_add_u32 v248, v248, 2, s18
	ds_read_b32 v248, v248
	s_waitcnt lgkmcnt(14)
	v_add_f32_e32 v90, v90, v249
	v_add_u32_e32 v249, v219, v207
	s_and_b64 vcc, s[8:9], s[90:91]
	v_cndmask_b32_e32 v249, v218, v249, vcc
	v_lshl_add_u32 v249, v249, 2, s18
	ds_read_b32 v249, v249
	s_waitcnt lgkmcnt(14)
	v_add_f32_e32 v91, v91, v250
	v_add_u32_e32 v250, v219, v208
	s_and_b64 vcc, s[8:9], s[92:93]
	v_cndmask_b32_e32 v250, v218, v250, vcc
	v_lshl_add_u32 v250, v250, 2, s18
	ds_read_b32 v250, v250
	s_waitcnt lgkmcnt(14)
	v_add_f32_e32 v92, v92, v251
	v_add_u32_e32 v251, v219, v209
	s_and_b64 vcc, s[8:9], s[94:95]
	v_cndmask_b32_e32 v251, v218, v251, vcc
	v_lshl_add_u32 v251, v251, 2, s18
	ds_read_b32 v251, v251
	s_waitcnt lgkmcnt(14)
	v_add_f32_e32 v93, v93, v252
	v_add_u32_e32 v252, v219, v210
	s_and_b64 vcc, s[8:9], s[96:97]
	v_cndmask_b32_e32 v252, v218, v252, vcc
	v_lshl_add_u32 v252, v252, 2, s18
	ds_read_b32 v252, v252
	s_waitcnt lgkmcnt(14)
	v_add_f32_e32 v94, v94, v253
	v_add_u32_e32 v253, v219, v211
	s_and_b64 vcc, s[8:9], s[2:3]
	v_cndmask_b32_e32 v253, v218, v253, vcc
	v_lshl_add_u32 v253, v253, 2, s18
	ds_read_b32 v253, v253
	s_waitcnt lgkmcnt(14)
	v_add_f32_e32 v95, v95, v220
	v_add_u32_e32 v220, v219, v212
	s_and_b64 vcc, s[8:9], s[0:1]
	v_cndmask_b32_e32 v220, v218, v220, vcc
	v_lshl_add_u32 v220, v220, 2, s18
	ds_read_b32 v220, v220
	s_waitcnt lgkmcnt(14)
	v_add_f32_e32 v64, v64, v221
	v_add_u32_e32 v221, v219, v213
	s_and_b64 vcc, s[8:9], s[6:7]
	v_cndmask_b32_e32 v221, v218, v221, vcc
	v_lshl_add_u32 v221, v221, 2, s18
	ds_read_b32 v221, v221
	s_waitcnt lgkmcnt(14)
	v_add_f32_e32 v65, v65, v241
	s_waitcnt lgkmcnt(13)
	v_add_f32_e32 v66, v66, v242
	s_waitcnt lgkmcnt(12)
	v_add_f32_e32 v67, v67, v243
	s_waitcnt lgkmcnt(11)
	v_add_f32_e32 v68, v68, v244
	s_waitcnt lgkmcnt(10)
	v_add_f32_e32 v69, v69, v245
	s_waitcnt lgkmcnt(9)
	v_add_f32_e32 v70, v70, v246
	s_waitcnt lgkmcnt(8)
	v_add_f32_e32 v71, v71, v247
	s_waitcnt lgkmcnt(7)
	v_add_f32_e32 v72, v72, v248
	s_waitcnt lgkmcnt(6)
	v_add_f32_e32 v73, v73, v249
	s_waitcnt lgkmcnt(5)
	v_add_f32_e32 v74, v74, v250
	s_waitcnt lgkmcnt(4)
	v_add_f32_e32 v75, v75, v251
	s_waitcnt lgkmcnt(3)
	v_add_f32_e32 v76, v76, v252
	s_waitcnt lgkmcnt(2)
	v_add_f32_e32 v77, v77, v253
	s_waitcnt lgkmcnt(1)
	v_add_f32_e32 v78, v78, v220
	s_waitcnt lgkmcnt(0)
	v_add_f32_e32 v79, v79, v221
.LBB0_618:
	ds_read_b64_tr_b16 v[242:243], v167 offset:0
	ds_read_b64_tr_b16 v[244:245], v167 offset:0x800
	ds_read_b64_tr_b16 v[246:247], v167 offset:0x1000
	ds_read_b64_tr_b16 v[248:249], v167 offset:0x1800
	ds_read_b64_tr_b16 v[250:251], v167 offset:0x2000
	ds_read_b64_tr_b16 v[252:253], v167 offset:0x2800
	ds_read_b64_tr_b16 v[218:219], v167 offset:0x3000
	ds_read_b64_tr_b16 v[220:221], v167 offset:0x3800
	s_waitcnt lgkmcnt(0)
	s_nop 0
	v_mfma_f32_32x32x16_bf16 v[0:15], v[144:147], v[242:245], v[0:15]
	v_mfma_f32_32x32x16_bf16 v[0:15], v[226:229], v[246:249], v[0:15]
	v_mfma_f32_32x32x16_bf16 v[0:15], v[230:233], v[250:253], v[0:15]
	v_mfma_f32_32x32x16_bf16 v[0:15], v[234:237], v[218:221], v[0:15]
	ds_read_b64_tr_b16 v[218:219], v167 offset:0x200
	ds_read_b64_tr_b16 v[220:221], v167 offset:0xa00
	ds_read_b64_tr_b16 v[242:243], v167 offset:0x1200
	ds_read_b64_tr_b16 v[244:245], v167 offset:0x1a00
	ds_read_b64_tr_b16 v[246:247], v167 offset:0x2200
	ds_read_b64_tr_b16 v[248:249], v167 offset:0x2a00
	ds_read_b64_tr_b16 v[250:251], v167 offset:0x3200
	ds_read_b64_tr_b16 v[252:253], v167 offset:0x3a00
	s_waitcnt lgkmcnt(0)
	s_nop 0
	v_mfma_f32_32x32x16_bf16 v[48:63], v[144:147], v[218:221], v[48:63]
	ds_read_b64_tr_b16 v[218:219], v167 offset:0x400
	ds_read_b64_tr_b16 v[220:221], v167 offset:0xc00
	v_mfma_f32_32x32x16_bf16 v[48:63], v[226:229], v[242:245], v[48:63]
	ds_read_b64_tr_b16 v[242:243], v167 offset:0x1400
	ds_read_b64_tr_b16 v[244:245], v167 offset:0x1c00
	v_mfma_f32_32x32x16_bf16 v[48:63], v[230:233], v[246:249], v[48:63]
	ds_read_b64_tr_b16 v[246:247], v167 offset:0x2400
	ds_read_b64_tr_b16 v[248:249], v167 offset:0x2c00
	v_mfma_f32_32x32x16_bf16 v[48:63], v[234:237], v[250:253], v[48:63]
	ds_read_b64_tr_b16 v[250:251], v167 offset:0x3400
	ds_read_b64_tr_b16 v[252:253], v167 offset:0x3c00
	s_waitcnt lgkmcnt(0)
	v_mfma_f32_32x32x16_bf16 v[32:47], v[144:147], v[218:221], v[32:47]
	ds_read_b64_tr_b16 v[218:219], v167 offset:0x600
	ds_read_b64_tr_b16 v[220:221], v167 offset:0xe00
	v_mfma_f32_32x32x16_bf16 v[32:47], v[226:229], v[242:245], v[32:47]
	ds_read_b64_tr_b16 v[242:243], v167 offset:0x1600
	ds_read_b64_tr_b16 v[244:245], v167 offset:0x1e00
	v_mfma_f32_32x32x16_bf16 v[32:47], v[230:233], v[246:249], v[32:47]
	ds_read_b64_tr_b16 v[246:247], v167 offset:0x2600
	ds_read_b64_tr_b16 v[248:249], v167 offset:0x2e00
	v_mfma_f32_32x32x16_bf16 v[32:47], v[234:237], v[250:253], v[32:47]
	ds_read_b64_tr_b16 v[250:251], v167 offset:0x3600
	ds_read_b64_tr_b16 v[252:253], v167 offset:0x3e00
	s_waitcnt lgkmcnt(0)
	v_mfma_f32_32x32x16_bf16 v[16:31], v[144:147], v[218:221], v[16:31]
	v_max_f32_e32 v144, v81, v81
	v_max_f32_e32 v145, v80, v80
	v_max_f32_e32 v144, v145, v144
	v_max3_f32 v144, v144, v82, v83
	v_max3_f32 v144, v144, v84, v85
	v_max3_f32 v144, v144, v86, v87
	v_max3_f32 v144, v144, v88, v89
	v_max3_f32 v144, v144, v90, v91
	v_max3_f32 v144, v144, v92, v93
	v_mfma_f32_32x32x16_bf16 v[16:31], v[226:229], v[242:245], v[16:31]
	v_max3_f32 v144, v144, v94, v95
	v_max3_f32 v144, v144, v64, v65
	v_max3_f32 v144, v144, v66, v67
	v_max3_f32 v144, v144, v68, v69
	v_max3_f32 v144, v144, v70, v71
	v_max3_f32 v144, v144, v72, v73
	v_max3_f32 v144, v144, v74, v75
	v_max3_f32 v144, v144, v76, v77
	v_mfma_f32_32x32x16_bf16 v[16:31], v[230:233], v[246:249], v[16:31]
	v_max3_f32 v144, v144, v78, v79
	v_mov_b32_e32 v145, v144
	s_nop 1
	v_permlane32_swap_b32_e32 v144, v145
	v_max_f32_e32 v145, v145, v145
	v_max_f32_e32 v144, v144, v144
	v_max_f32_e32 v144, v144, v145
	v_sub_f32_e32 v145, v144, v222
	s_mov_b32 s8, 0x42b504f3
	v_cmp_ge_f32_e32 vcc, s8, v145
	v_max_f32_e32 v145, v222, v222
	v_max_f32_e32 v145, v145, v144
	v_mfma_f32_32x32x16_bf16 v[16:31], v[234:237], v[250:253], v[16:31]
	v_sub_f32_e32 v144, v222, v145
	v_mul_f32_e32 v144, 0x3e0293ee, v144
	v_exp_f32_e32 v144, v144
	s_cmp_eq_u64 vcc, exec
	s_cselect_b64 s[8:9], -1, 0
	s_barrier
	s_waitcnt vmcnt(0)
	v_cndmask_b32_e64 v144, v144, 1.0, s[8:9]
	v_cmp_gt_f32_e32 vcc, 1.0, v144
	s_waitcnt vmcnt(3)
	ds_write_b128 v156, v[128:131] offset:16384
	s_waitcnt vmcnt(2)
	ds_write_b128 v157, v[132:135] offset:16384
	s_waitcnt vmcnt(1)
	ds_write_b128 v153, v[136:139] offset:49152
	s_waitcnt vmcnt(0)
	ds_write_b128 v155, v[140:143] offset:49152
	s_cbranch_vccz .LBB0_622
	s_and_saveexec_b64 s[10:11], s[4:5]
	ds_write_b32 v171, v144 offset:128
	s_or_b64 exec, exec, s[10:11]
	s_waitcnt lgkmcnt(0)
	v_add_u32_e32 v140, v159, v148
	ds_read_b128 v[128:131], v140 offset:224
	ds_read_b128 v[132:135], v140 offset:192
	ds_read_b128 v[136:139], v140 offset:160
	ds_read_b128 v[140:143], v140 offset:128
	s_waitcnt lgkmcnt(3)
	v_pk_mul_f32 v[12:13], v[12:13], v[128:129]
	s_waitcnt lgkmcnt(2)
	v_pk_mul_f32 v[8:9], v[8:9], v[132:133]
	s_waitcnt lgkmcnt(1)
	v_pk_mul_f32 v[4:5], v[4:5], v[136:137]
	v_pk_mul_f32 v[14:15], v[14:15], v[130:131]
	v_pk_mul_f32 v[10:11], v[10:11], v[134:135]
	v_pk_mul_f32 v[6:7], v[6:7], v[138:139]
	s_waitcnt lgkmcnt(0)
	v_pk_mul_f32 v[2:3], v[2:3], v[142:143]
	v_pk_mul_f32 v[0:1], v[0:1], v[140:141]
	v_pk_mul_f32 v[60:61], v[60:61], v[128:129]
	v_pk_mul_f32 v[56:57], v[56:57], v[132:133]
	v_pk_mul_f32 v[52:53], v[52:53], v[136:137]
	v_pk_mul_f32 v[62:63], v[62:63], v[130:131]
	v_pk_mul_f32 v[58:59], v[58:59], v[134:135]
	v_pk_mul_f32 v[54:55], v[54:55], v[138:139]
	v_pk_mul_f32 v[50:51], v[50:51], v[142:143]
	v_pk_mul_f32 v[48:49], v[48:49], v[140:141]
	v_pk_mul_f32 v[44:45], v[44:45], v[128:129]
	v_pk_mul_f32 v[40:41], v[40:41], v[132:133]
	v_pk_mul_f32 v[36:37], v[36:37], v[136:137]
	v_pk_mul_f32 v[46:47], v[46:47], v[130:131]
	v_pk_mul_f32 v[42:43], v[42:43], v[134:135]
	v_pk_mul_f32 v[38:39], v[38:39], v[138:139]
	v_pk_mul_f32 v[34:35], v[34:35], v[142:143]
	v_pk_mul_f32 v[32:33], v[32:33], v[140:141]
	v_pk_mul_f32 v[28:29], v[28:29], v[128:129]
	v_pk_mul_f32 v[24:25], v[24:25], v[132:133]
	v_pk_mul_f32 v[20:21], v[20:21], v[136:137]
	v_pk_mul_f32 v[30:31], v[30:31], v[130:131]
	v_pk_mul_f32 v[26:27], v[26:27], v[134:135]
	v_pk_mul_f32 v[22:23], v[22:23], v[138:139]
	v_pk_mul_f32 v[18:19], v[18:19], v[142:143]
	v_pk_mul_f32 v[16:17], v[16:17], v[140:141]

.LBB0_695:
	global_load_dwordx4 v[28:31], v[44:45], off offset:-4096
	global_load_dwordx4 v[24:27], v[44:45], off offset:-3072
	global_load_dwordx4 v[20:23], v[44:45], off offset:-2048
	global_load_dwordx4 v[12:15], v[44:45], off
	global_load_dwordx4 v[16:19], v[44:45], off offset:2048
	global_load_dwordx4 v[0:3], v[44:45], off offset:-1024
	global_load_dwordx4 v[4:7], v[44:45], off offset:1024
	global_load_dwordx4 v[8:11], v[44:45], off offset:3072
	s_waitcnt vmcnt(7)
	v_max_f32_e64 v53, |v31|, |v31|
	v_max_f32_e64 v54, |v30|, |v30|
	v_max_f32_e32 v53, v54, v53
	v_max3_f32 v55, |v28|, |v29|, v53
	s_waitcnt vmcnt(6)
	v_max_f32_e64 v53, |v27|, |v27|
	v_max_f32_e64 v54, |v26|, |v26|
	v_max_f32_e32 v53, v54, v53
	v_max3_f32 v53, |v24|, |v25|, v53
	v_max3_f32 v56, v55, 0, v53
	s_waitcnt vmcnt(5)
	v_max_f32_e64 v53, |v23|, |v23|
	v_max_f32_e64 v54, |v22|, |v22|
	v_max_f32_e32 v53, v54, v53
	v_max3_f32 v57, |v20|, |v21|, v53
	s_waitcnt vmcnt(4)
	v_max_f32_e64 v53, |v15|, |v15|
	v_max_f32_e64 v54, |v14|, |v14|
	v_max_f32_e32 v53, v54, v53
	v_max3_f32 v59, |v12|, |v13|, v53
	s_waitcnt vmcnt(3)
	v_max_f32_e64 v53, |v19|, |v19|
	v_max_f32_e64 v54, |v18|, |v18|
	v_max_f32_e32 v53, v54, v53
	v_max3_f32 v60, |v16|, |v17|, v53
	s_waitcnt vmcnt(2)
	v_max_f32_e64 v53, |v3|, |v3|
	v_max_f32_e64 v54, |v2|, |v2|
	v_max_f32_e32 v53, v54, v53
	v_max3_f32 v55, |v0|, |v1|, v53
	v_max3_f32 v58, v56, v57, v55
	s_waitcnt vmcnt(1)
	v_max_f32_e64 v53, |v7|, |v7|
	v_max_f32_e64 v54, |v6|, |v6|
	v_max_f32_e32 v53, v54, v53
	v_max3_f32 v55, |v4|, |v5|, v53
	v_max3_f32 v37, v58, v59, v55
	s_waitcnt vmcnt(0)
	v_max_f32_e64 v53, |v11|, |v11|
	v_max_f32_e64 v54, |v10|, |v10|
	v_max_f32_e32 v53, v54, v53
	v_max3_f32 v55, |v8|, |v9|, v53
	v_max3_f32 v37, v37, v60, v55
	s_nop 1
	v_mov_b32_dpp v48, v37 quad_perm:[1,0,3,2] row_mask:0xf bank_mask:0xf bound_ctrl:1
	v_max_f32_e32 v48, v48, v48
	v_max_f32_e32 v37, v37, v48
	s_nop 1
	v_mov_b32_dpp v48, v37 quad_perm:[2,3,0,1] row_mask:0xf bank_mask:0xf bound_ctrl:1
	v_max_f32_e32 v48, v48, v48
	v_max_f32_e32 v37, v37, v48
	s_nop 1
	v_mov_b32_dpp v48, v37 row_half_mirror row_mask:0xf bank_mask:0xf bound_ctrl:1
	v_max_f32_e32 v48, v48, v48
	v_max_f32_e32 v37, v37, v48
	s_nop 1
	v_mov_b32_dpp v48, v37 row_mirror row_mask:0xf bank_mask:0xf bound_ctrl:1
	v_max_f32_e32 v48, v48, v48
	v_max_f32_e32 v37, v37, v48
	ds_swizzle_b32 v48, v37 offset:swizzle(SWAP,16)
	s_waitcnt lgkmcnt(0)
	v_max_f32_e32 v48, v48, v48
	v_max_f32_e32 v37, v37, v48
	s_nop 0
	v_readlane_b32 s7, v37, 0
	v_readlane_b32 s17, v37, 32
	s_nop 0
	v_max_f32_e64 v48, s7, s7
	v_max_f32_e64 v37, s17, s17
	v_max_f32_e32 v37, v48, v37
	v_cmp_lt_f32_e32 vcc, 0, v37
	v_mul_f32_e32 v37, 0x3c010204, v37
	s_mov_b32 s17, 0x40c0c00
	v_cndmask_b32_e32 v37, 1.0, v37, vcc
	v_div_scale_f32 v48, s[18:19], v37, v37, 1.0
	v_rcp_f32_e32 v49, v48
	s_mov_b32 s7, 0x30600000
	v_fma_f32 v50, -v48, v49, 1.0
	v_fmac_f32_e32 v49, v50, v49
	v_div_scale_f32 v50, vcc, 1.0, v37, 1.0
	v_mul_f32_e32 v51, v50, v49
	v_fma_f32 v52, -v48, v51, v50
	v_fmac_f32_e32 v51, v52, v49
	v_fma_f32 v48, -v48, v51, v50
	v_div_fmas_f32 v48, v48, v49, v51
	v_div_fixup_f32 v48, v48, v37, 1.0
	v_mul_f32_e32 v29, v29, v48
	v_mul_f32_e32 v28, v28, v48
	v_rndne_f32_e32 v29, v29
	v_mul_f32_e32 v30, v30, v48
	v_mul_f32_e32 v31, v31, v48
	v_mul_f32_e32 v25, v25, v48
	v_rndne_f32_e32 v28, v28
	v_cvt_i32_f32_e32 v29, v29
	v_rndne_f32_e32 v30, v30
	v_rndne_f32_e32 v31, v31
	v_mul_f32_e32 v24, v24, v48
	v_rndne_f32_e32 v25, v25
	v_mul_f32_e32 v26, v26, v48
	v_mul_f32_e32 v27, v27, v48
	v_cvt_i32_f32_e32 v28, v28
	v_cvt_i32_f32_sdwa v30, v30 dst_sel:WORD_1 dst_unused:UNUSED_PAD src0_sel:DWORD
	v_cvt_i32_f32_e32 v31, v31
	v_rndne_f32_e32 v24, v24
	v_cvt_i32_f32_e32 v25, v25
	v_rndne_f32_e32 v26, v26
	v_rndne_f32_e32 v27, v27
	v_cvt_i32_f32_e32 v24, v24
	v_cvt_i32_f32_sdwa v26, v26 dst_sel:WORD_1 dst_unused:UNUSED_PAD src0_sel:DWORD
	v_cvt_i32_f32_e32 v27, v27
	v_mul_f32_e32 v21, v21, v48
	v_mul_f32_e32 v20, v20, v48
	v_rndne_f32_e32 v21, v21
	v_mul_f32_e32 v22, v22, v48
	v_mul_f32_e32 v23, v23, v48
	v_lshlrev_b32_e32 v29, 8, v29
	v_rndne_f32_e32 v20, v20
	v_cvt_i32_f32_e32 v21, v21
	v_rndne_f32_e32 v22, v22
	v_rndne_f32_e32 v23, v23
	v_mul_f32_e32 v1, v1, v48
	v_and_b32_e32 v29, 0xff00, v29
	v_and_b32_e32 v30, 0xff0000, v30
	v_perm_b32 v28, v31, v28, s17
	v_lshlrev_b32_e32 v25, 8, v25
	v_cvt_i32_f32_e32 v20, v20
	v_cvt_i32_f32_sdwa v22, v22 dst_sel:WORD_1 dst_unused:UNUSED_PAD src0_sel:DWORD
	v_cvt_i32_f32_e32 v23, v23
	v_mul_f32_e32 v0, v0, v48
	v_rndne_f32_e32 v1, v1
	v_mul_f32_e32 v2, v2, v48
	v_mul_f32_e32 v3, v3, v48
	v_or3_b32 v30, v28, v29, v30
	v_lshl_add_u64 v[28:29], v[42:43], 0, v[192:193]
	v_and_b32_e32 v25, 0xff00, v25
	v_and_b32_e32 v26, 0xff0000, v26
	v_perm_b32 v24, v27, v24, s17
	v_rndne_f32_e32 v0, v0
	v_cvt_i32_f32_e32 v1, v1
	v_rndne_f32_e32 v2, v2
	v_rndne_f32_e32 v3, v3
	global_store_dword v[28:29], v30, off
	v_or3_b32 v28, v24, v25, v26
	v_lshl_add_u64 v[24:25], v[40:41], 0, v[192:193]
	v_cvt_i32_f32_e32 v0, v0
	v_cvt_i32_f32_sdwa v2, v2 dst_sel:WORD_1 dst_unused:UNUSED_PAD src0_sel:DWORD
	v_cvt_i32_f32_e32 v3, v3
	v_add_co_u32_e32 v26, vcc, s7, v24
	v_lshlrev_b32_e32 v21, 8, v21
	s_nop 0
	v_addc_co_u32_e32 v27, vcc, 0, v25, vcc
	v_and_b32_e32 v21, 0xff00, v21
	v_and_b32_e32 v22, 0xff0000, v22
	v_perm_b32 v20, v23, v20, s17
	s_mov_b32 s7, 0x30a00000
	v_or3_b32 v22, v20, v21, v22
	v_add_co_u32_e32 v20, vcc, s7, v24
	v_lshlrev_b32_e32 v1, 8, v1
	s_nop 0
	v_addc_co_u32_e32 v21, vcc, 0, v25, vcc
	v_and_b32_e32 v1, 0xff00, v1
	v_and_b32_e32 v2, 0xff0000, v2
	v_perm_b32 v0, v3, v0, s17
	s_mov_b32 s7, 0x30e00000
	v_or3_b32 v2, v0, v1, v2
	v_add_co_u32_e32 v0, vcc, s7, v24
	v_mul_f32_e32 v3, v15, v48
	s_nop 0
	v_addc_co_u32_e32 v1, vcc, 0, v25, vcc
	global_store_dword v[0:1], v2, off
	v_mul_f32_e32 v1, v13, v48
	v_mul_f32_e32 v0, v12, v48
	v_rndne_f32_e32 v1, v1
	v_mul_f32_e32 v2, v14, v48
	v_rndne_f32_e32 v0, v0
	v_cvt_i32_f32_e32 v1, v1
	v_rndne_f32_e32 v2, v2
	v_rndne_f32_e32 v3, v3
	v_cvt_i32_f32_e32 v0, v0
	v_cvt_i32_f32_sdwa v2, v2 dst_sel:WORD_1 dst_unused:UNUSED_PAD src0_sel:DWORD
	v_cvt_i32_f32_e32 v3, v3
	v_lshlrev_b32_e32 v1, 8, v1
	v_and_b32_e32 v1, 0xff00, v1
	v_and_b32_e32 v2, 0xff0000, v2
	v_perm_b32 v0, v3, v0, s17
	s_mov_b32 s7, 0x31200000
	v_or3_b32 v2, v0, v1, v2
	v_add_co_u32_e32 v0, vcc, s7, v24
	v_mul_f32_e32 v3, v7, v48
	s_nop 0
	v_addc_co_u32_e32 v1, vcc, 0, v25, vcc
	global_store_dword v[0:1], v2, off
	v_mul_f32_e32 v1, v5, v48
	v_mul_f32_e32 v0, v4, v48
	v_rndne_f32_e32 v1, v1
	v_mul_f32_e32 v2, v6, v48
	v_rndne_f32_e32 v0, v0
	v_cvt_i32_f32_e32 v1, v1
	v_rndne_f32_e32 v2, v2
	v_rndne_f32_e32 v3, v3
	v_cvt_i32_f32_e32 v0, v0
	v_cvt_i32_f32_sdwa v2, v2 dst_sel:WORD_1 dst_unused:UNUSED_PAD src0_sel:DWORD
	v_cvt_i32_f32_e32 v3, v3
	v_lshlrev_b32_e32 v1, 8, v1
	v_and_b32_e32 v1, 0xff00, v1
	v_and_b32_e32 v2, 0xff0000, v2
	v_perm_b32 v0, v3, v0, s17
	s_mov_b32 s7, 0x31600000
	v_or3_b32 v2, v0, v1, v2
	v_add_co_u32_e32 v0, vcc, s7, v24
	v_mul_f32_e32 v3, v19, v48
	s_nop 0
	v_addc_co_u32_e32 v1, vcc, 0, v25, vcc
	global_store_dword v[0:1], v2, off
	v_mul_f32_e32 v1, v17, v48
	v_mul_f32_e32 v0, v16, v48
	v_rndne_f32_e32 v1, v1
	v_mul_f32_e32 v2, v18, v48
	v_rndne_f32_e32 v0, v0
	v_cvt_i32_f32_e32 v1, v1
	v_rndne_f32_e32 v2, v2
	v_rndne_f32_e32 v3, v3
	v_cvt_i32_f32_e32 v0, v0
	v_cvt_i32_f32_sdwa v2, v2 dst_sel:WORD_1 dst_unused:UNUSED_PAD src0_sel:DWORD
	v_cvt_i32_f32_e32 v3, v3
	v_lshlrev_b32_e32 v1, 8, v1
	v_and_b32_e32 v1, 0xff00, v1
	v_and_b32_e32 v2, 0xff0000, v2
	v_perm_b32 v0, v3, v0, s17
	s_mov_b32 s7, 0x31a00000
	v_or3_b32 v2, v0, v1, v2
	v_add_co_u32_e32 v0, vcc, s7, v24
	v_mul_f32_e32 v3, v11, v48
	s_nop 0
	v_addc_co_u32_e32 v1, vcc, 0, v25, vcc
	global_store_dword v[0:1], v2, off
	v_mul_f32_e32 v1, v9, v48
	v_mul_f32_e32 v0, v8, v48
	v_rndne_f32_e32 v1, v1
	v_mul_f32_e32 v2, v10, v48
	v_rndne_f32_e32 v0, v0
	v_cvt_i32_f32_e32 v1, v1
	v_rndne_f32_e32 v2, v2
	v_rndne_f32_e32 v3, v3
	v_cvt_i32_f32_e32 v0, v0
	v_cvt_i32_f32_sdwa v2, v2 dst_sel:WORD_1 dst_unused:UNUSED_PAD src0_sel:DWORD
	v_cvt_i32_f32_e32 v3, v3
	v_lshlrev_b32_e32 v1, 8, v1
	v_and_b32_e32 v1, 0xff00, v1
	v_and_b32_e32 v2, 0xff0000, v2
	v_perm_b32 v0, v3, v0, s17
	v_or3_b32 v2, v0, v1, v2
	v_add_co_u32_e32 v0, vcc, 0x31e00000, v24
	global_store_dword v[26:27], v28, off
	s_nop 0
	v_addc_co_u32_e32 v1, vcc, 0, v25, vcc
	global_store_dword v[20:21], v22, off
	global_store_dword v[0:1], v2, off
	s_and_saveexec_b64 s[18:19], s[2:3]
	s_cbranch_execz .LBB0_694
	global_store_dword v[38:39], v37, off
	s_branch .LBB0_694

.LBB0_700:
	global_load_dwordx4 v[28:31], v[38:39], off offset:-4096
	global_load_dwordx4 v[24:27], v[38:39], off offset:-3072
	global_load_dwordx4 v[20:23], v[38:39], off offset:-2048
	global_load_dwordx4 v[12:15], v[38:39], off
	global_load_dwordx4 v[16:19], v[38:39], off offset:2048
	global_load_dwordx4 v[0:3], v[38:39], off offset:-1024
	global_load_dwordx4 v[4:7], v[38:39], off offset:1024
	global_load_dwordx4 v[8:11], v[38:39], off offset:3072
	s_waitcnt vmcnt(7)
	v_max_f32_e64 v53, |v31|, |v31|
	v_max_f32_e64 v54, |v30|, |v30|
	v_max_f32_e32 v53, v54, v53
	v_max3_f32 v55, |v28|, |v29|, v53
	s_waitcnt vmcnt(6)
	v_max_f32_e64 v53, |v27|, |v27|
	v_max_f32_e64 v54, |v26|, |v26|
	v_max_f32_e32 v53, v54, v53
	v_max3_f32 v53, |v24|, |v25|, v53
	v_max3_f32 v56, v55, 0, v53
	s_waitcnt vmcnt(5)
	v_max_f32_e64 v53, |v23|, |v23|
	v_max_f32_e64 v54, |v22|, |v22|
	v_max_f32_e32 v53, v54, v53
	v_max3_f32 v57, |v20|, |v21|, v53
	s_waitcnt vmcnt(4)
	v_max_f32_e64 v53, |v15|, |v15|
	v_max_f32_e64 v54, |v14|, |v14|
	v_max_f32_e32 v53, v54, v53
	v_max3_f32 v59, |v12|, |v13|, v53
	s_waitcnt vmcnt(3)
	v_max_f32_e64 v53, |v19|, |v19|
	v_max_f32_e64 v54, |v18|, |v18|
	v_max_f32_e32 v53, v54, v53
	v_max3_f32 v60, |v16|, |v17|, v53
	s_waitcnt vmcnt(2)
	v_max_f32_e64 v53, |v3|, |v3|
	v_max_f32_e64 v54, |v2|, |v2|
	v_max_f32_e32 v53, v54, v53
	v_max3_f32 v55, |v0|, |v1|, v53
	v_max3_f32 v58, v56, v57, v55
	s_waitcnt vmcnt(1)
	v_max_f32_e64 v53, |v7|, |v7|
	v_max_f32_e64 v54, |v6|, |v6|
	v_max_f32_e32 v53, v54, v53
	v_max3_f32 v55, |v4|, |v5|, v53
	v_max3_f32 v40, v58, v59, v55
	s_waitcnt vmcnt(0)
	v_max_f32_e64 v53, |v11|, |v11|
	v_max_f32_e64 v54, |v10|, |v10|
	v_max_f32_e32 v53, v54, v53
	v_max3_f32 v55, |v8|, |v9|, v53
	v_max3_f32 v40, v40, v60, v55
	s_nop 1
	v_mov_b32_dpp v41, v40 quad_perm:[1,0,3,2] row_mask:0xf bank_mask:0xf bound_ctrl:1
	v_max_f32_e32 v41, v41, v41
	v_max_f32_e32 v40, v40, v41
	s_nop 1
	v_mov_b32_dpp v41, v40 quad_perm:[2,3,0,1] row_mask:0xf bank_mask:0xf bound_ctrl:1
	v_max_f32_e32 v41, v41, v41
	v_max_f32_e32 v40, v40, v41
	s_nop 1
	v_mov_b32_dpp v41, v40 row_half_mirror row_mask:0xf bank_mask:0xf bound_ctrl:1
	v_max_f32_e32 v41, v41, v41
	v_max_f32_e32 v40, v40, v41
	s_nop 1
	v_mov_b32_dpp v41, v40 row_mirror row_mask:0xf bank_mask:0xf bound_ctrl:1
	v_max_f32_e32 v41, v41, v41
	v_max_f32_e32 v40, v40, v41
	ds_swizzle_b32 v41, v40 offset:swizzle(SWAP,16)
	s_waitcnt lgkmcnt(0)
	v_max_f32_e32 v41, v41, v41
	v_max_f32_e32 v40, v40, v41
	s_nop 0
	v_readlane_b32 s5, v40, 0
	v_readlane_b32 s14, v40, 32
	s_nop 0
	v_max_f32_e64 v41, s5, s5
	v_max_f32_e64 v40, s14, s14
	v_max_f32_e32 v40, v41, v40
	v_cmp_lt_f32_e32 vcc, 0, v40
	v_mul_f32_e32 v40, 0x3c010204, v40
	s_mov_b32 s5, 0x32600000
	v_cndmask_b32_e32 v40, 1.0, v40, vcc
	v_div_scale_f32 v41, s[14:15], v40, v40, 1.0
	v_rcp_f32_e32 v42, v41
	s_mov_b32 s14, 0x40c0c00
	v_fma_f32 v43, -v41, v42, 1.0
	v_fmac_f32_e32 v42, v43, v42
	v_div_scale_f32 v43, vcc, 1.0, v40, 1.0
	v_mul_f32_e32 v44, v43, v42
	v_fma_f32 v45, -v41, v44, v43
	v_fmac_f32_e32 v44, v45, v42
	v_fma_f32 v41, -v41, v44, v43
	v_div_fmas_f32 v41, v41, v42, v44
	v_div_fixup_f32 v41, v41, v40, 1.0
	v_mul_f32_e32 v29, v29, v41
	v_mul_f32_e32 v28, v28, v41
	v_rndne_f32_e32 v29, v29
	v_mul_f32_e32 v30, v30, v41
	v_mul_f32_e32 v31, v31, v41
	v_mul_f32_e32 v25, v25, v41
	v_rndne_f32_e32 v28, v28
	v_cvt_i32_f32_e32 v29, v29
	v_rndne_f32_e32 v30, v30
	v_rndne_f32_e32 v31, v31
	v_mul_f32_e32 v24, v24, v41
	v_rndne_f32_e32 v25, v25
	v_mul_f32_e32 v26, v26, v41
	v_mul_f32_e32 v27, v27, v41
	v_cvt_i32_f32_e32 v28, v28
	v_cvt_i32_f32_sdwa v30, v30 dst_sel:WORD_1 dst_unused:UNUSED_PAD src0_sel:DWORD
	v_cvt_i32_f32_e32 v31, v31
	v_rndne_f32_e32 v24, v24
	v_cvt_i32_f32_e32 v25, v25
	v_rndne_f32_e32 v26, v26
	v_rndne_f32_e32 v27, v27
	v_cvt_i32_f32_e32 v24, v24
	v_cvt_i32_f32_sdwa v26, v26 dst_sel:WORD_1 dst_unused:UNUSED_PAD src0_sel:DWORD
	v_cvt_i32_f32_e32 v27, v27
	v_mul_f32_e32 v21, v21, v41
	v_mul_f32_e32 v20, v20, v41
	v_rndne_f32_e32 v21, v21
	v_mul_f32_e32 v22, v22, v41
	v_mul_f32_e32 v23, v23, v41
	v_lshlrev_b32_e32 v29, 8, v29
	v_rndne_f32_e32 v20, v20
	v_cvt_i32_f32_e32 v21, v21
	v_rndne_f32_e32 v22, v22
	v_rndne_f32_e32 v23, v23
	v_mul_f32_e32 v1, v1, v41
	v_and_b32_e32 v29, 0xff00, v29
	v_and_b32_e32 v30, 0xff0000, v30
	v_perm_b32 v28, v31, v28, s14
	v_lshlrev_b32_e32 v25, 8, v25
	v_cvt_i32_f32_e32 v20, v20
	v_cvt_i32_f32_sdwa v22, v22 dst_sel:WORD_1 dst_unused:UNUSED_PAD src0_sel:DWORD
	v_cvt_i32_f32_e32 v23, v23
	v_mul_f32_e32 v0, v0, v41
	v_rndne_f32_e32 v1, v1
	v_mul_f32_e32 v2, v2, v41
	v_mul_f32_e32 v3, v3, v41
	v_or3_b32 v30, v28, v29, v30
	v_lshl_add_u64 v[28:29], v[32:33], 0, v[192:193]
	v_and_b32_e32 v25, 0xff00, v25
	v_and_b32_e32 v26, 0xff0000, v26
	v_perm_b32 v24, v27, v24, s14
	v_rndne_f32_e32 v0, v0
	v_cvt_i32_f32_e32 v1, v1
	v_rndne_f32_e32 v2, v2
	v_rndne_f32_e32 v3, v3
	global_store_dword v[28:29], v30, off
	v_or3_b32 v28, v24, v25, v26
	v_lshl_add_u64 v[24:25], v[36:37], 0, v[192:193]
	v_cvt_i32_f32_e32 v0, v0
	v_cvt_i32_f32_sdwa v2, v2 dst_sel:WORD_1 dst_unused:UNUSED_PAD src0_sel:DWORD
	v_cvt_i32_f32_e32 v3, v3
	v_add_co_u32_e32 v26, vcc, s5, v24
	v_lshlrev_b32_e32 v21, 8, v21
	s_nop 0
	v_addc_co_u32_e32 v27, vcc, 0, v25, vcc
	v_and_b32_e32 v21, 0xff00, v21
	v_and_b32_e32 v22, 0xff0000, v22
	v_perm_b32 v20, v23, v20, s14
	s_mov_b32 s5, 0x32a00000
	v_or3_b32 v22, v20, v21, v22
	v_add_co_u32_e32 v20, vcc, s5, v24
	v_lshlrev_b32_e32 v1, 8, v1
	s_nop 0
	v_addc_co_u32_e32 v21, vcc, 0, v25, vcc
	v_and_b32_e32 v1, 0xff00, v1
	v_and_b32_e32 v2, 0xff0000, v2
	v_perm_b32 v0, v3, v0, s14
	s_mov_b32 s5, 0x32e00000
	v_or3_b32 v2, v0, v1, v2
	v_add_co_u32_e32 v0, vcc, s5, v24
	v_mul_f32_e32 v3, v15, v41
	s_nop 0
	v_addc_co_u32_e32 v1, vcc, 0, v25, vcc
	global_store_dword v[0:1], v2, off
	v_mul_f32_e32 v1, v13, v41
	v_mul_f32_e32 v0, v12, v41
	v_rndne_f32_e32 v1, v1
	v_mul_f32_e32 v2, v14, v41
	v_rndne_f32_e32 v0, v0
	v_cvt_i32_f32_e32 v1, v1
	v_rndne_f32_e32 v2, v2
	v_rndne_f32_e32 v3, v3
	v_cvt_i32_f32_e32 v0, v0
	v_cvt_i32_f32_sdwa v2, v2 dst_sel:WORD_1 dst_unused:UNUSED_PAD src0_sel:DWORD
	v_cvt_i32_f32_e32 v3, v3
	v_lshlrev_b32_e32 v1, 8, v1
	v_and_b32_e32 v1, 0xff00, v1
	v_and_b32_e32 v2, 0xff0000, v2
	v_perm_b32 v0, v3, v0, s14
	s_mov_b32 s5, 0x33200000
	v_or3_b32 v2, v0, v1, v2
	v_add_co_u32_e32 v0, vcc, s5, v24
	v_mul_f32_e32 v3, v7, v41
	s_nop 0
	v_addc_co_u32_e32 v1, vcc, 0, v25, vcc
	global_store_dword v[0:1], v2, off
	v_mul_f32_e32 v1, v5, v41
	v_mul_f32_e32 v0, v4, v41
	v_rndne_f32_e32 v1, v1
	v_mul_f32_e32 v2, v6, v41
	v_rndne_f32_e32 v0, v0
	v_cvt_i32_f32_e32 v1, v1
	v_rndne_f32_e32 v2, v2
	v_rndne_f32_e32 v3, v3
	v_cvt_i32_f32_e32 v0, v0
	v_cvt_i32_f32_sdwa v2, v2 dst_sel:WORD_1 dst_unused:UNUSED_PAD src0_sel:DWORD
	v_cvt_i32_f32_e32 v3, v3
	v_lshlrev_b32_e32 v1, 8, v1
	v_and_b32_e32 v1, 0xff00, v1
	v_and_b32_e32 v2, 0xff0000, v2
	v_perm_b32 v0, v3, v0, s14
	s_mov_b32 s5, 0x33600000
	v_or3_b32 v2, v0, v1, v2
	v_add_co_u32_e32 v0, vcc, s5, v24
	v_mul_f32_e32 v3, v19, v41
	s_nop 0
	v_addc_co_u32_e32 v1, vcc, 0, v25, vcc
	global_store_dword v[0:1], v2, off
	v_mul_f32_e32 v1, v17, v41
	v_mul_f32_e32 v0, v16, v41
	v_rndne_f32_e32 v1, v1
	v_mul_f32_e32 v2, v18, v41
	v_rndne_f32_e32 v0, v0
	v_cvt_i32_f32_e32 v1, v1
	v_rndne_f32_e32 v2, v2
	v_rndne_f32_e32 v3, v3
	v_cvt_i32_f32_e32 v0, v0
	v_cvt_i32_f32_sdwa v2, v2 dst_sel:WORD_1 dst_unused:UNUSED_PAD src0_sel:DWORD
	v_cvt_i32_f32_e32 v3, v3
	v_lshlrev_b32_e32 v1, 8, v1
	v_and_b32_e32 v1, 0xff00, v1
	v_and_b32_e32 v2, 0xff0000, v2
	v_perm_b32 v0, v3, v0, s14
	s_mov_b32 s5, 0x33a00000
	v_or3_b32 v2, v0, v1, v2
	v_add_co_u32_e32 v0, vcc, s5, v24
	v_mul_f32_e32 v3, v11, v41
	s_nop 0
	v_addc_co_u32_e32 v1, vcc, 0, v25, vcc
	global_store_dword v[0:1], v2, off
	v_mul_f32_e32 v1, v9, v41
	v_mul_f32_e32 v0, v8, v41
	v_rndne_f32_e32 v1, v1
	v_mul_f32_e32 v2, v10, v41
	v_rndne_f32_e32 v0, v0
	v_cvt_i32_f32_e32 v1, v1
	v_rndne_f32_e32 v2, v2
	v_rndne_f32_e32 v3, v3
	v_cvt_i32_f32_e32 v0, v0
	v_cvt_i32_f32_sdwa v2, v2 dst_sel:WORD_1 dst_unused:UNUSED_PAD src0_sel:DWORD
	v_cvt_i32_f32_e32 v3, v3
	v_lshlrev_b32_e32 v1, 8, v1
	v_and_b32_e32 v1, 0xff00, v1
	v_and_b32_e32 v2, 0xff0000, v2
	v_perm_b32 v0, v3, v0, s14
	v_or3_b32 v2, v0, v1, v2
	v_add_co_u32_e32 v0, vcc, 0x33e00000, v24
	global_store_dword v[26:27], v28, off
	s_nop 0
	v_addc_co_u32_e32 v1, vcc, 0, v25, vcc
	global_store_dword v[20:21], v22, off
	global_store_dword v[0:1], v2, off
	s_and_saveexec_b64 s[14:15], s[0:1]
	s_cbranch_execz .LBB0_699
	global_store_dword v[34:35], v40, off
	s_branch .LBB0_699
